# baseline (speedup 1.0000x reference)
.LBB1_2:
	s_load_dwordx8 s[4:11], s[0:1], 0x0
	s_lshr_b32 s0, s2, 3
	s_bfe_u32 s33, s2, 0x30003
	v_readfirstlane_b32 s36, v0
	s_mov_b32 s57, 0
	s_nop 0
	s_mov_b32 s54, s36
	s_and_b32 s3, s2, 7
	s_and_b32 s0, s0, 8
	s_xor_b32 s44, s33, 15
	s_bfe_u32 s38, s36, 0x20006
	s_or_b32 s14, s0, s3
	s_lshr_b32 s30, s2, 7
	s_mov_b32 s31, 0
	s_lshl_b32 s0, s44, 7
	s_lshl_b32 s39, s38, 5
	s_lshl_b64 s[18:19], s[30:31], 11
	s_or_b32 s0, s39, s0
	s_or_b32 s0, s18, s0
	s_mov_b32 s1, s19
	s_lshr_b32 s35, s36, 6
	s_lshr_b32 s37, s36, 8
	s_lshl_b64 s[12:13], s[0:1], 11
	s_waitcnt lgkmcnt(0)
	s_add_u32 s12, s4, s12
	s_addc_u32 s13, s5, s13
	s_lshl_b32 s42, s14, 6
	s_lshl_b32 s14, s14, 7
	s_add_u32 s16, s12, s14
	s_addc_u32 s17, s13, 0
	s_lshl_b64 s[12:13], s[30:31], 22
	s_add_u32 s6, s6, s12
	s_addc_u32 s7, s7, s13
	s_add_u32 s6, s6, s14
	s_addc_u32 s7, s7, 0
	s_lshr_b32 s15, s36, 4
	v_and_b32_e32 v200, 7, v0
	v_bfe_u32 v208, v0, 4, 2
	s_and_b32 s15, s15, 4
	v_bfe_u32 v193, v0, 3, 3
	v_bitop3_b32 v1, s15, v200, v208 bitop3:0x36
	s_add_u32 s15, s8, s12
	v_lshl_or_b32 v188, s35, 3, v193
	v_mov_b32_e32 v189, 0
	s_addc_u32 s20, s9, s13
	v_lshlrev_b64 v[2:3], 11, v[188:189]
	v_lshlrev_b32_e32 v188, 4, v1
	s_add_u32 s14, s15, s14
	v_lshlrev_b32_e32 v1, 8, v0
	v_lshl_add_u64 v[2:3], s[6:7], 0, v[2:3]
	s_addc_u32 s15, s20, 0
	s_lshl_b32 s34, s38, 14
	v_and_b32_e32 v1, 0x3c00, v1
	v_lshl_add_u64 v[194:195], v[2:3], 0, v[188:189]
	v_or_b32_e32 v2, s34, v1
	s_lshl_b32 s30, s37, 6
	s_lshl_b32 s20, s35, 10
	v_lshlrev_b32_e32 v188, 1, v2
	v_lshlrev_b32_e32 v4, 3, v0
	s_cmp_lg_u32 0, -1
	v_lshl_add_u64 v[2:3], s[14:15], 0, v[188:189]
	v_and_b32_e32 v209, 24, v4
	s_cselect_b32 s21, 0, 0
	v_lshl_add_u64 v[2:3], v[2:3], 0, s[30:31]
	v_lshlrev_b32_e32 v190, 1, v209
	v_mov_b32_e32 v191, v189
	s_add_i32 s41, s20, s21
	s_bitcmp1_b32 s54, 8
	s_cbranch_scc1 .Ldmaskip_1
	s_mov_b32 s21, m0
	s_mov_b32 m0, s41
	s_nop 0
	global_load_lds_dwordx4 v[194:195], off
	s_mov_b32 m0, s21
	s_cmp_ge_u32 s41, 0xc000
	s_cselect_b32 s56, 64, 0x10000
	v_lshl_add_u64 v[220:221], v[194:195], 0, s[56:57]
	s_add_i32 s55, s41, 0x1000
	s_mov_b32 m0, s55
	s_nop 0
	global_load_lds_dwordx4 v[220:221], off
.Ldmaskip_1:
	s_mov_b64 s[22:23], 0x20000
	v_lshl_add_u64 v[196:197], v[2:3], 0, v[190:191]
	v_lshl_add_u64 v[2:3], v[194:195], 0, s[22:23]
	s_add_i32 s21, s41, 0x2000
	s_bitcmp1_b32 s54, 8
	s_cbranch_scc1 .Ldmaskip_2
	s_mov_b32 s24, m0
	s_mov_b32 m0, s21
	s_nop 0
	global_load_lds_dwordx4 v[2:3], off
	s_mov_b32 m0, s24
	s_cmp_ge_u32 s21, 0xc000
	s_cselect_b32 s56, 64, 0x10000
	v_lshl_add_u64 v[220:221], v[2:3], 0, s[56:57]
	s_add_i32 s55, s21, 0x1000
	s_mov_b32 m0, s55
	s_nop 0
	global_load_lds_dwordx4 v[220:221], off
.Ldmaskip_2:
	s_add_i32 s40, s41, 0xc000
	s_bitcmp1_b32 s54, 8
	s_cbranch_scc1 .Ldmaskip_3
	s_mov_b32 s24, m0
	s_mov_b32 m0, s40
	s_nop 0
	global_load_lds_dwordx4 v[196:197], off
	s_mov_b32 m0, s24
	s_cmp_ge_u32 s40, 0xc000
	s_cselect_b32 s56, 64, 0x10000
	v_lshl_add_u64 v[220:221], v[196:197], 0, s[56:57]
	s_add_i32 s55, s40, 0x1000
	s_mov_b32 m0, s55
	s_nop 0
	global_load_lds_dwordx4 v[220:221], off
.Ldmaskip_3:
	v_lshl_add_u64 v[198:199], v[196:197], 0, s[22:23]
	s_add_i32 s24, s40, 0x2000
	s_bitcmp1_b32 s54, 8
	s_cbranch_scc1 .Ldmaskip_4
	s_mov_b32 s25, m0
	s_mov_b32 m0, s24
	s_nop 0
	global_load_lds_dwordx4 v[198:199], off
	s_mov_b32 m0, s25
	s_cmp_ge_u32 s24, 0xc000
	s_cselect_b32 s56, 64, 0x10000
	v_lshl_add_u64 v[220:221], v[198:199], 0, s[56:57]
	s_add_i32 s55, s24, 0x1000
	s_mov_b32 m0, s55
	s_nop 0
	global_load_lds_dwordx4 v[220:221], off
.Ldmaskip_4:
	s_mov_b64 s[24:25], 0x40000
	v_lshl_add_u64 v[2:3], v[194:195], 0, s[24:25]
	s_add_i32 s26, s41, 0x4000
	s_bitcmp1_b32 s54, 8
	s_cbranch_scc1 .Ldmaskip_5
	s_mov_b32 s27, m0
	s_mov_b32 m0, s26
	s_nop 0
	global_load_lds_dwordx4 v[2:3], off
	s_mov_b32 m0, s27
	s_cmp_ge_u32 s26, 0xc000
	s_cselect_b32 s56, 64, 0x10000
	v_lshl_add_u64 v[220:221], v[2:3], 0, s[56:57]
	s_add_i32 s55, s26, 0x1000
	s_mov_b32 m0, s55
	s_nop 0
	global_load_lds_dwordx4 v[220:221], off
.Ldmaskip_5:
	s_mov_b64 s[26:27], 0x60000
	v_and_b32_e32 v202, 31, v0
	v_lshl_add_u64 v[2:3], v[194:195], 0, s[26:27]
	v_bfe_u32 v201, v0, 5, 1
	s_add_i32 s28, s41, 0x6000
	s_bitcmp1_b32 s54, 8
	s_cbranch_scc1 .Ldmaskip_6
	s_mov_b32 s29, m0
	s_mov_b32 m0, s28
	s_nop 0
	global_load_lds_dwordx4 v[2:3], off
	s_mov_b32 m0, s29
	s_cmp_ge_u32 s28, 0xc000
	s_cselect_b32 s56, 64, 0x10000
	v_lshl_add_u64 v[220:221], v[2:3], 0, s[56:57]
	s_add_i32 s55, s28, 0x1000
	s_mov_b32 m0, s55
	s_nop 0
	global_load_lds_dwordx4 v[220:221], off
.Ldmaskip_6:
	v_lshlrev_b32_e32 v2, 10, v202
	v_lshl_or_b32 v2, v201, 3, v2
	v_lshlrev_b32_e32 v216, 1, v2
	global_load_dwordx4 v[144:147], v216, s[16:17]
	global_load_dwordx4 v[140:143], v216, s[16:17] offset:32
	global_load_dwordx4 v[136:139], v216, s[16:17] offset:64
	global_load_dwordx4 v[132:135], v216, s[16:17] offset:96
	s_lshl_b32 s28, s37, 13
	v_lshrrev_b32_e32 v2, 1, v0
	s_add_i32 s30, s28, 0
	v_bitop3_b32 v2, v201, v2, 7 bitop3:0x78
	s_mov_b64 s[28:29], 0x80000
	v_lshlrev_b32_e32 v207, 4, v2
	v_lshl_add_u64 v[2:3], v[194:195], 0, s[28:29]
	s_add_i32 s16, s41, 0x8000
	s_bitcmp1_b32 s54, 8
	s_cbranch_scc1 .Ldmaskip_7
	s_mov_b32 s17, m0
	s_mov_b32 m0, s16
	s_nop 0
	global_load_lds_dwordx4 v[2:3], off
	s_mov_b32 m0, s17
	s_cmp_ge_u32 s16, 0xc000
	s_cselect_b32 s56, 64, 0x10000
	v_lshl_add_u64 v[220:221], v[2:3], 0, s[56:57]
	s_add_i32 s55, s16, 0x1000
	s_mov_b32 m0, s55
	s_nop 0
	global_load_lds_dwordx4 v[220:221], off
.Ldmaskip_7:
	v_lshlrev_b32_e32 v211, 7, v202
	s_mov_b64 s[16:17], 0xa0000
	v_add_u32_e32 v217, s30, v211
	v_lshl_add_u64 v[2:3], v[194:195], 0, s[16:17]
	s_add_i32 s16, s41, 0xa000
	s_bitcmp1_b32 s54, 8
	s_cbranch_scc1 .Ldmaskip_8
	s_mov_b32 s17, m0
	s_mov_b32 m0, s16
	s_nop 0
	global_load_lds_dwordx4 v[2:3], off
	s_mov_b32 m0, s17
	s_cmp_ge_u32 s16, 0xc000
	s_cselect_b32 s56, 64, 0x10000
	v_lshl_add_u64 v[220:221], v[2:3], 0, s[56:57]
	s_add_i32 s55, s16, 0x1000
	s_mov_b32 m0, s55
	s_nop 0
	global_load_lds_dwordx4 v[220:221], off
.Ldmaskip_8:
	s_waitcnt vmcnt(8) lgkmcnt(0)
	s_barrier
	v_add_u32_e32 v70, v217, v207
	ds_read_b128 v[2:5], v70
	ds_read_b128 v[18:21], v70 offset:4096
	v_xor_b32_e32 v206, 32, v207
	v_add_u32_e32 v71, v217, v206
	ds_read_b128 v[22:25], v71
	ds_read_b128 v[34:37], v71 offset:4096
	v_xor_b32_e32 v205, 64, v207
	s_waitcnt vmcnt(3) lgkmcnt(3)
	v_mfma_f32_32x32x16_f16 v[2:17], v[2:5], v[144:147], 0
	v_add_u32_e32 v72, v217, v205
	v_xor_b32_e32 v204, 0x60, v207
	v_add_u32_e32 v73, v217, v204
	s_mov_b32 s46, 5
	s_movk_i32 s48, 0x4000
	s_mov_b32 s45, 0x8000
	v_and_b32_e32 v212, 63, v0
	s_waitcnt vmcnt(2) lgkmcnt(1)
	v_mfma_f32_32x32x16_f16 v[2:17], v[22:25], v[140:143], v[2:17]
	v_mfma_f32_32x32x16_f16 v[18:33], v[18:21], v[144:147], 0
	s_waitcnt lgkmcnt(0)
	v_mfma_f32_32x32x16_f16 v[18:33], v[34:37], v[140:143], v[18:33]
	ds_read_b128 v[34:37], v72
	ds_read_b128 v[38:41], v72 offset:4096
	s_waitcnt vmcnt(1) lgkmcnt(1)
	v_mfma_f32_32x32x16_f16 v[2:17], v[34:37], v[136:139], v[2:17]
	s_waitcnt lgkmcnt(0)
	v_mfma_f32_32x32x16_f16 v[18:33], v[38:41], v[136:139], v[18:33]
	ds_read_b128 v[34:37], v73
	ds_read_b128 v[38:41], v73 offset:4096
	s_waitcnt vmcnt(0) lgkmcnt(1)
	v_mfma_f32_32x32x16_f16 v[2:17], v[34:37], v[132:135], v[2:17]
	s_waitcnt lgkmcnt(0)
	v_mfma_f32_32x32x16_f16 v[18:33], v[38:41], v[132:135], v[18:33]
	s_nop 9
	v_max_f32_e64 v35, |v2|, |v2|
	s_nop 0
	v_max_f32_e64 v34, |v18|, |v18|
	v_min_f32_e32 v34, v35, v34
	v_min3_f32 v34, v34, |v3|, |v19|
	v_min3_f32 v34, v34, |v4|, |v20|
	v_min3_f32 v34, v34, |v5|, |v21|
	v_min3_f32 v34, v34, |v6|, |v22|
	v_min3_f32 v34, v34, |v7|, |v23|
	v_min3_f32 v34, v34, |v8|, |v24|
	v_min3_f32 v34, v34, |v9|, |v25|
	v_min3_f32 v34, v34, |v10|, |v26|
	v_min3_f32 v34, v34, |v11|, |v27|
	v_min3_f32 v34, v34, |v12|, |v28|
	v_min3_f32 v34, v34, |v13|, |v29|
	v_min3_f32 v34, v34, |v14|, |v30|
	v_min3_f32 v34, v34, |v15|, |v31|
	v_min3_f32 v34, v34, |v16|, |v32|
	v_min3_f32 v34, v34, |v17|, |v33|
	v_cmp_eq_f32_e32 vcc, 0, v34
	s_cbranch_vccnz .LBB1_114
.LBB1_3:
	v_lshlrev_b32_e32 v34, 5, v208
	v_lshlrev_b32_e32 v203, 2, v201
	v_lshrrev_b32_e32 v35, 2, v0
	v_and_b32_e32 v191, 32, v34
	v_and_or_b32 v35, v35, 3, v203
	v_add_u32_e32 v34, s30, v191
	v_lshlrev_b32_e32 v210, 6, v35
	v_add3_u32 v215, v34, v209, v210
	v_max_f32_e32 v34, v3, v3
	v_max_f32_e32 v35, v2, v2
	v_max_f32_e32 v34, v35, v34
	v_max3_f32 v35, v4, v5, v19
	v_max3_f32 v34, v34, v18, v20
	v_max3_f32 v34, v34, v21, v6
	v_max3_f32 v35, v35, v8, v9
	v_max3_f32 v34, v34, v7, v22
	v_max3_f32 v35, v35, v24, v25
	v_max3_f32 v34, v34, v23, v10
	v_max3_f32 v35, v35, v12, v13
	v_max3_f32 v34, v34, v11, v26
	v_max3_f32 v35, v35, v28, v29
	v_max3_f32 v34, v34, v27, v14
	v_max3_f32 v35, v35, v16, v17
	v_max3_f32 v34, v34, v15, v30
	v_max3_f32 v35, v35, v32, v33
	v_max3_f32 v34, v34, v31, v35
	v_mov_b32_e32 v35, v34
	s_lshl_b64 s[16:17], s[0:1], 10
	s_and_b32 s0, s36, 0x3fffffc0
	v_permlane32_swap_b32_e32 v34, v35
	s_lshl_b32 s0, s0, 2
	v_max_f32_e32 v35, v35, v35
	v_max_f32_e32 v34, v34, v34
	s_add_i32 s0, s0, 0
	v_max_f32_e32 v34, v34, v35
	s_mov_b32 s47, 0x41000000
	s_add_i32 s30, s0, 0x18000
	v_cmp_le_f32_e32 vcc, -4.0, v34
	v_cmp_ge_f32_e64 s[0:1], s47, v34
	v_max_f32_e32 v34, 0xf149f2ca, v34
	s_and_b64 s[0:1], vcc, s[0:1]
	v_cndmask_b32_e64 v192, v34, 0, s[0:1]
	v_add_f32_e64 v2, v2, -v192
	v_exp_f32_e32 v50, v2
	v_add_f32_e64 v2, v18, -v192
	v_exp_f32_e32 v34, v2
	v_add_f32_e64 v2, v3, -v192
	v_exp_f32_e32 v51, v2
	v_add_f32_e64 v2, v19, -v192
	v_exp_f32_e32 v35, v2
	v_add_f32_e64 v2, v4, -v192
	v_exp_f32_e32 v52, v2
	v_add_f32_e64 v2, v20, -v192
	v_exp_f32_e32 v36, v2
	v_add_f32_e64 v2, v5, -v192
	v_exp_f32_e32 v53, v2
	v_add_f32_e64 v2, v21, -v192
	v_exp_f32_e32 v37, v2
	v_add_f32_e64 v2, v6, -v192
	v_exp_f32_e32 v54, v2
	v_add_f32_e64 v2, v22, -v192
	v_exp_f32_e32 v38, v2
	v_add_f32_e64 v2, v7, -v192
	v_exp_f32_e32 v55, v2
	v_add_f32_e64 v2, v23, -v192
	v_exp_f32_e32 v39, v2
	v_add_f32_e64 v2, v8, -v192
	v_exp_f32_e32 v56, v2
	v_add_f32_e64 v2, v24, -v192
	v_exp_f32_e32 v40, v2
	v_add_f32_e64 v2, v9, -v192
	v_exp_f32_e32 v57, v2
	v_add_f32_e64 v2, v25, -v192
	v_exp_f32_e32 v41, v2
	v_add_f32_e64 v2, v10, -v192
	v_exp_f32_e32 v58, v2
	v_add_f32_e64 v2, v26, -v192
	v_exp_f32_e32 v42, v2
	v_add_f32_e64 v2, v11, -v192
	v_exp_f32_e32 v59, v2
	v_add_f32_e64 v2, v27, -v192
	v_exp_f32_e32 v43, v2
	v_add_f32_e64 v2, v12, -v192
	v_exp_f32_e32 v60, v2
	v_add_f32_e64 v2, v28, -v192
	v_exp_f32_e32 v44, v2
	v_add_f32_e64 v2, v13, -v192
	v_exp_f32_e32 v61, v2
	v_add_f32_e64 v2, v29, -v192
	v_exp_f32_e32 v45, v2
	v_add_f32_e64 v2, v14, -v192
	v_exp_f32_e32 v62, v2
	v_add_f32_e64 v2, v30, -v192
	v_exp_f32_e32 v46, v2
	v_add_f32_e64 v2, v15, -v192
	v_exp_f32_e32 v63, v2
	v_add_f32_e64 v2, v31, -v192
	v_exp_f32_e32 v47, v2
	v_add_f32_e64 v2, v16, -v192
	v_exp_f32_e32 v64, v2
	v_add_f32_e64 v2, v32, -v192
	v_exp_f32_e32 v48, v2
	v_add_f32_e64 v2, v17, -v192
	v_exp_f32_e32 v65, v2
	v_add_f32_e64 v2, v33, -v192
	s_waitcnt vmcnt(0) lgkmcnt(0)
	s_barrier
	s_mov_b64 s[0:1], 0xc0000
	v_exp_f32_e32 v49, v2
	v_lshl_add_u64 v[2:3], v[194:195], 0, s[0:1]
	s_bitcmp1_b32 s54, 8
	s_cbranch_scc1 .Ldmaskip_9
	s_mov_b32 s0, m0
	s_mov_b32 m0, s41
	s_nop 0
	global_load_lds_dwordx4 v[2:3], off
	s_mov_b32 m0, s0
	s_cmp_ge_u32 s41, 0xc000
	s_cselect_b32 s56, 64, 0x10000
	v_lshl_add_u64 v[220:221], v[2:3], 0, s[56:57]
	s_add_i32 s55, s41, 0x1000
	s_mov_b32 m0, s55
	s_nop 0
	global_load_lds_dwordx4 v[220:221], off
.Ldmaskip_9:
	s_mov_b64 s[0:1], 0xe0000
	v_lshl_add_u64 v[2:3], v[194:195], 0, s[0:1]
	s_bitcmp1_b32 s54, 8
	s_cbranch_scc1 .Ldmaskip_10
	s_mov_b32 s0, m0
	s_mov_b32 m0, s21
	s_nop 0
	global_load_lds_dwordx4 v[2:3], off
	s_mov_b32 m0, s0
	s_cmp_ge_u32 s21, 0xc000
	s_cselect_b32 s56, 64, 0x10000
	v_lshl_add_u64 v[220:221], v[2:3], 0, s[56:57]
	s_add_i32 s55, s21, 0x1000
	s_mov_b32 m0, s55
	s_nop 0
	global_load_lds_dwordx4 v[220:221], off
.Ldmaskip_10:
	s_cmp_lg_u32 0, -1
	s_cselect_b32 s0, 0, 0
	s_add_i32 s0, s0, s20
	v_cmp_neq_f32_e32 vcc, 0, v192
	v_lshl_add_u64 v[2:3], v[196:197], 0, s[24:25]
	s_add_i32 s1, s0, 0x10000
	s_bitcmp1_b32 s54, 8
	s_cbranch_scc1 .Ldmaskip_11
	s_mov_b32 s20, m0
	s_mov_b32 m0, s1
	s_nop 0
	global_load_lds_dwordx4 v[2:3], off
	s_mov_b32 m0, s20
	s_cmp_ge_u32 s1, 0xc000
	s_cselect_b32 s56, 64, 0x10000
	v_lshl_add_u64 v[220:221], v[2:3], 0, s[56:57]
	s_add_i32 s55, s1, 0x1000
	s_mov_b32 m0, s55
	s_nop 0
	global_load_lds_dwordx4 v[220:221], off
.Ldmaskip_11:
	s_add_i32 s0, s0, 0x12000
	v_lshl_add_u64 v[2:3], v[196:197], 0, s[26:27]
	s_bitcmp1_b32 s54, 8
	s_cbranch_scc1 .Ldmaskip_12
	s_mov_b32 s1, m0
	s_mov_b32 m0, s0
	s_nop 0
	global_load_lds_dwordx4 v[2:3], off
	s_mov_b32 m0, s1
	s_cmp_ge_u32 s0, 0xc000
	s_cselect_b32 s56, 64, 0x10000
	v_lshl_add_u64 v[220:221], v[2:3], 0, s[56:57]
	s_add_i32 s55, s0, 0x1000
	s_mov_b32 m0, s55
	s_nop 0
	global_load_lds_dwordx4 v[220:221], off
.Ldmaskip_12:
	s_cmp_eq_u64 vcc, 0
	ds_read_b128 v[66:69], v70 offset:16384
	ds_read_b128 v[82:85], v70 offset:20480
	ds_read_b128 v[168:171], v71 offset:16384
	ds_read_b128 v[164:167], v71 offset:20480
	ds_read_b128 v[160:163], v72 offset:16384
	ds_read_b128 v[156:159], v72 offset:20480
	ds_read_b128 v[152:155], v73 offset:16384
	ds_read_b128 v[148:151], v73 offset:20480
	s_cselect_b64 s[20:21], -1, 0
	s_lshr_b32 s43, s36, 2
	s_and_b32 s43, s43, 0x3fffffc0
	s_add_u32 s43, s12, s43
	s_addc_u32 s49, s13, 0
	s_lshl_b32 s2, s2, 4
	v_and_b32_e32 v2, 3, v0
	s_lshl_b32 s3, s3, 7
	s_and_b32 s2, s2, 0x400
	v_lshlrev_b32_e32 v188, 4, v2
	v_add_lshl_u32 v4, s34, v1, 1
	s_or_b32 s34, s2, s3
	v_or_b32_e32 v2, s43, v188
	v_mov_b32_e32 v3, s49
	v_mov_b32_e32 v5, v189
	s_add_u32 s2, s8, s34
	v_lshl_add_u64 v[2:3], v[2:3], 0, v[4:5]
	s_addc_u32 s3, s9, 0
	s_waitcnt vmcnt(8) lgkmcnt(0)
	s_barrier
	v_lshl_add_u64 v[2:3], s[2:3], 0, v[2:3]
	v_mov_b32_e32 v18, v189
	v_mov_b32_e32 v19, v189
	v_lshl_add_u64 v[126:127], v[2:3], 0, s[28:29]
	v_mov_b32_e32 v20, v189
	v_mov_b32_e32 v21, v189
	v_mov_b32_e32 v22, v189
	v_mov_b32_e32 v23, v189
	v_mov_b32_e32 v24, v189
	v_mov_b32_e32 v25, v189
	v_mov_b32_e32 v26, v189
	v_mov_b32_e32 v27, v189
	v_mov_b32_e32 v28, v189
	v_mov_b32_e32 v29, v189
	v_mov_b32_e32 v30, v189
	v_mov_b32_e32 v31, v189
	v_mov_b32_e32 v32, v189
	v_mov_b32_e32 v33, v189
	v_mov_b64_e32 v[2:3], v[18:19]
	v_cmp_gt_u32_e64 s[0:1], 32, v212
	v_lshl_add_u32 v214, v202, 2, s30
	v_lshl_add_u32 v213, v201, 4, s30
	v_mov_b32_e32 v180, 0xff800000
	v_mov_b32_e32 v218, v189
	v_mov_b64_e32 v[4:5], v[20:21]
	v_mov_b64_e32 v[6:7], v[22:23]
	v_mov_b64_e32 v[8:9], v[24:25]
	v_mov_b64_e32 v[10:11], v[26:27]
	v_mov_b64_e32 v[12:13], v[28:29]
	v_mov_b64_e32 v[14:15], v[30:31]
	v_mov_b64_e32 v[16:17], v[32:33]
.LBB1_4:
	v_mfma_f32_32x32x16_f16 v[66:81], v[66:69], v[144:147], 0
	v_add_u32_e32 v181, s31, v215
	ds_read_b64_tr_b16 v[172:173], v181 offset:49152
	ds_read_b64_tr_b16 v[174:175], v181 offset:49664
	v_add_f32_e32 v86, v50, v51
	v_add_f32_e32 v86, v52, v86
	v_add_f32_e32 v86, v53, v86
	v_add_f32_e32 v86, v54, v86
	v_add_f32_e32 v86, v55, v86
	s_waitcnt lgkmcnt(9)
	v_cvt_pk_f16_f32 v128, v50, v51
	v_cvt_pk_f16_f32 v129, v52, v53
	s_nop 0
	ds_read_b64_tr_b16 v[176:177], v181 offset:53248
	ds_read_b64_tr_b16 v[178:179], v181 offset:53760
	v_add_f32_e32 v50, v56, v86
	s_waitcnt lgkmcnt(10)
	v_mfma_f32_32x32x16_f16 v[82:97], v[82:85], v[144:147], 0
	v_add_f32_e32 v50, v57, v50
	v_add_f32_e32 v50, v58, v50
	v_add_f32_e32 v50, v59, v50
	v_cvt_pk_f16_f32 v130, v54, v55
	v_cvt_pk_f16_f32 v131, v56, v57
	s_nop 0
	ds_read_b64_tr_b16 v[122:123], v181 offset:50176
	ds_read_b64_tr_b16 v[124:125], v181 offset:50688
	s_waitcnt lgkmcnt(11)
	v_mfma_f32_32x32x16_f16 v[66:81], v[168:171], v[140:143], v[66:81]
	v_add_f32_e32 v50, v60, v50
	v_add_f32_e32 v50, v61, v50
	v_add_f32_e32 v50, v62, v50
	v_add_f32_e32 v50, v63, v50
	v_cvt_pk_f16_f32 v106, v58, v59
	v_cvt_pk_f16_f32 v107, v60, v61
	s_nop 0
	ds_read_b64_tr_b16 v[118:119], v181 offset:54272
	ds_read_b64_tr_b16 v[120:121], v181 offset:54784
	s_waitcnt lgkmcnt(12)
	v_mfma_f32_32x32x16_f16 v[82:97], v[164:167], v[140:143], v[82:97]
	v_add_f32_e32 v50, v64, v50
	v_add_f32_e32 v50, v65, v50
	v_add_f32_e32 v50, v34, v50
	v_add_f32_e32 v50, v35, v50
	v_cvt_pk_f16_f32 v108, v62, v63
	v_cvt_pk_f16_f32 v109, v64, v65
	s_nop 0
	ds_read_b64_tr_b16 v[114:115], v181 offset:51200
	ds_read_b64_tr_b16 v[116:117], v181 offset:51712
	s_waitcnt lgkmcnt(13)
	v_mfma_f32_32x32x16_f16 v[66:81], v[160:163], v[136:139], v[66:81]
	v_add_f32_e32 v50, v36, v50
	v_add_f32_e32 v50, v37, v50
	v_add_f32_e32 v50, v38, v50
	v_add_f32_e32 v50, v39, v50
	v_cvt_pk_f16_f32 v102, v34, v35
	v_cvt_pk_f16_f32 v103, v36, v37
	s_nop 0
	ds_read_b64_tr_b16 v[110:111], v181 offset:55296
	ds_read_b64_tr_b16 v[112:113], v181 offset:55808
	s_waitcnt lgkmcnt(14)
	v_mfma_f32_32x32x16_f16 v[82:97], v[156:159], v[136:139], v[82:97]
	v_add_f32_e32 v34, v40, v50
	v_add_f32_e32 v34, v41, v34
	v_add_f32_e32 v34, v42, v34
	v_add_f32_e32 v34, v43, v34
	v_cvt_pk_f16_f32 v104, v38, v39
	v_cvt_pk_f16_f32 v105, v40, v41
	s_nop 0
	ds_read_b64_tr_b16 v[156:157], v181 offset:52224
	ds_read_b64_tr_b16 v[158:159], v181 offset:52736
	s_waitcnt lgkmcnt(14)
	v_mfma_f32_32x32x16_f16 v[66:81], v[152:155], v[132:135], v[66:81]
	v_add_f32_e32 v34, v44, v34
	v_add_f32_e32 v34, v45, v34
	v_add_f32_e32 v34, v46, v34
	v_add_f32_e32 v34, v47, v34
	v_cvt_pk_f16_f32 v98, v42, v43
	v_cvt_pk_f16_f32 v99, v44, v45
	s_nop 0
	ds_read_b64_tr_b16 v[152:153], v181 offset:56320
	ds_read_b64_tr_b16 v[154:155], v181 offset:56832
	v_mfma_f32_32x32x16_f16 v[82:97], v[148:151], v[132:135], v[82:97]
	v_add_f32_e32 v34, v48, v34
	v_add_f32_e32 v34, v49, v34
	v_add_f32_e32 v160, 0, v34
	v_cvt_pk_f16_f32 v100, v46, v47
	v_cvt_pk_f16_f32 v101, v48, v49
	s_nop 0
	s_add_i32 s49, s33, s46
	s_sub_i32 s3, s49, 17
	s_add_i32 s2, s46, -1
	s_min_i32 s3, s3, s33
	s_cmp_gt_u32 s2, s44
	s_cselect_b32 s2, s3, s2
	s_ashr_i32 s3, s2, 31
	s_lshl_b64 s[2:3], s[2:3], 18
	v_lshl_add_u64 v[34:35], v[194:195], 0, s[2:3]
	s_add_i32 s2, s48, s41
	s_bitcmp1_b32 s54, 8
	s_cbranch_scc1 .Ldmaskip_13
	s_mov_b32 s3, m0
	s_mov_b32 m0, s2
	s_nop 0
	global_load_lds_dwordx4 v[34:35], off
	s_mov_b32 m0, s3
	s_cmp_ge_u32 s2, 0xc000
	s_cselect_b32 s56, 64, 0x10000
	v_lshl_add_u64 v[220:221], v[34:35], 0, s[56:57]
	s_add_i32 s55, s2, 0x1000
	s_mov_b32 m0, s55
	s_nop 0
	global_load_lds_dwordx4 v[220:221], off
.Ldmaskip_13:
	v_lshl_add_u64 v[34:35], v[34:35], 0, s[22:23]
	s_addk_i32 s2, 0x2000
	s_bitcmp1_b32 s54, 8
	s_cbranch_scc1 .Ldmaskip_14
	s_mov_b32 s3, m0
	s_mov_b32 m0, s2
	s_nop 0
	global_load_lds_dwordx4 v[34:35], off
	s_mov_b32 m0, s3
	s_cmp_ge_u32 s2, 0xc000
	s_cselect_b32 s56, 64, 0x10000
	v_lshl_add_u64 v[220:221], v[34:35], 0, s[56:57]
	s_add_i32 s55, s2, 0x1000
	s_mov_b32 m0, s55
	s_nop 0
	global_load_lds_dwordx4 v[220:221], off
.Ldmaskip_14:
	s_add_i32 s2, s45, s40
	s_bitcmp1_b32 s54, 8
	s_cbranch_scc1 .Ldmaskip_15
	s_mov_b32 s3, m0
	s_mov_b32 m0, s2
	s_nop 0
	global_load_lds_dwordx4 v[126:127], off
	s_mov_b32 m0, s3
	s_cmp_ge_u32 s2, 0xc000
	s_cselect_b32 s56, 64, 0x10000
	v_lshl_add_u64 v[220:221], v[126:127], 0, s[56:57]
	s_add_i32 s55, s2, 0x1000
	s_mov_b32 m0, s55
	s_nop 0
	global_load_lds_dwordx4 v[220:221], off
.Ldmaskip_15:
	v_lshl_add_u64 v[34:35], v[126:127], 0, s[22:23]
	s_addk_i32 s2, 0x2000
	s_bitcmp1_b32 s54, 8
	s_cbranch_scc1 .Ldmaskip_16
	s_mov_b32 s3, m0
	s_mov_b32 m0, s2
	s_nop 0
	global_load_lds_dwordx4 v[34:35], off
	s_mov_b32 m0, s3
	s_cmp_ge_u32 s2, 0xc000
	s_cselect_b32 s56, 64, 0x10000
	v_lshl_add_u64 v[220:221], v[34:35], 0, s[56:57]
	s_add_i32 s55, s2, 0x1000
	s_mov_b32 m0, s55
	s_nop 0
	global_load_lds_dwordx4 v[220:221], off
.Ldmaskip_16:
	s_and_b64 vcc, exec, s[20:21]
	s_mov_b64 s[2:3], -1
	s_cbranch_vccz .LBB1_20
	s_andn2_b64 vcc, exec, s[2:3]
	s_cbranch_vccnz .LBB1_8

.LBB1_9:
	s_xor_b64 s[30:31], s[20:21], -1
	s_waitcnt lgkmcnt(14)
	v_mfma_f32_32x32x16_f16 v[18:33], v[128:131], v[172:175], v[18:33]
	v_exp_f32_e32 v66, v66
	v_exp_f32_e32 v67, v67
	v_exp_f32_e32 v68, v68
	v_exp_f32_e32 v69, v69
	s_waitcnt lgkmcnt(12)
	v_mfma_f32_32x32x16_f16 v[2:17], v[128:131], v[176:179], v[2:17]
	v_exp_f32_e32 v70, v70
	v_exp_f32_e32 v71, v71
	v_exp_f32_e32 v72, v72
	v_exp_f32_e32 v73, v73
	v_add_u32_e32 v54, s45, v217
	v_add_u32_e32 v55, v54, v207
	ds_read_b128 v[50:53], v55
	ds_read_b128 v[34:37], v55 offset:4096
	s_waitcnt lgkmcnt(12)
	v_mfma_f32_32x32x16_f16 v[18:33], v[106:109], v[122:125], v[18:33]
	v_exp_f32_e32 v74, v74
	v_exp_f32_e32 v75, v75
	v_exp_f32_e32 v76, v76
	v_exp_f32_e32 v77, v77
	v_add_u32_e32 v55, v54, v206
	ds_read_b128 v[122:125], v55
	ds_read_b128 v[172:175], v55 offset:4096
	s_waitcnt lgkmcnt(12)
	v_mfma_f32_32x32x16_f16 v[2:17], v[106:109], v[118:121], v[2:17]
	v_exp_f32_e32 v78, v78
	v_exp_f32_e32 v79, v79
	v_exp_f32_e32 v80, v80
	v_exp_f32_e32 v81, v81
	v_add_u32_e32 v55, v54, v205
	ds_read_b128 v[176:179], v55
	ds_read_b128 v[164:167], v55 offset:4096
	s_waitcnt lgkmcnt(12)
	v_mfma_f32_32x32x16_f16 v[18:33], v[102:105], v[114:117], v[18:33]
	v_exp_f32_e32 v82, v82
	v_exp_f32_e32 v83, v83
	v_exp_f32_e32 v84, v84
	v_exp_f32_e32 v85, v85
	v_add_u32_e32 v54, v54, v204
	ds_read_b128 v[168:171], v54
	ds_read_b128 v[160:163], v54 offset:4096
	s_waitcnt lgkmcnt(12)
	v_mfma_f32_32x32x16_f16 v[2:17], v[102:105], v[110:113], v[2:17]
	v_exp_f32_e32 v86, v86
	v_exp_f32_e32 v87, v87
	v_exp_f32_e32 v88, v88
	v_exp_f32_e32 v89, v89
	s_waitcnt lgkmcnt(10)
	v_mfma_f32_32x32x16_f16 v[18:33], v[98:101], v[156:159], v[18:33]
	v_exp_f32_e32 v90, v90
	v_exp_f32_e32 v91, v91
	v_exp_f32_e32 v92, v92
	v_exp_f32_e32 v93, v93
	s_waitcnt lgkmcnt(8)
	v_mfma_f32_32x32x16_f16 v[2:17], v[98:101], v[152:155], v[2:17]
	v_exp_f32_e32 v94, v94
	v_exp_f32_e32 v95, v95
	v_exp_f32_e32 v96, v96
	v_exp_f32_e32 v97, v97
	s_waitcnt vmcnt(8) lgkmcnt(0)
	s_barrier
	s_andn2_b64 vcc, exec, s[2:3]
	s_cbranch_vccnz .LBB1_11
	ds_read_b128 v[54:57], v213 offset:96
	ds_read_b128 v[58:61], v213 offset:64
	ds_read_b128 v[62:65], v213 offset:32
	ds_read_b128 v[38:41], v213
	s_waitcnt lgkmcnt(3)
	v_pk_mul_f32 v[32:33], v[32:33], v[56:57]
	s_waitcnt lgkmcnt(2)
	v_pk_mul_f32 v[28:29], v[28:29], v[60:61]
	s_waitcnt lgkmcnt(1)
	v_pk_mul_f32 v[24:25], v[24:25], v[64:65]
	s_waitcnt lgkmcnt(0)
	v_pk_mul_f32 v[20:21], v[20:21], v[40:41]
	v_pk_mul_f32 v[30:31], v[30:31], v[54:55]
	v_pk_mul_f32 v[26:27], v[26:27], v[58:59]
	v_pk_mul_f32 v[22:23], v[22:23], v[62:63]
	v_pk_mul_f32 v[18:19], v[18:19], v[38:39]
	v_pk_mul_f32 v[16:17], v[16:17], v[56:57]
	v_pk_mul_f32 v[12:13], v[12:13], v[60:61]
	v_pk_mul_f32 v[8:9], v[8:9], v[64:65]
	v_pk_mul_f32 v[4:5], v[4:5], v[40:41]
	v_pk_mul_f32 v[14:15], v[14:15], v[54:55]
	v_pk_mul_f32 v[10:11], v[10:11], v[58:59]
	v_pk_mul_f32 v[6:7], v[6:7], v[62:63]
	v_pk_mul_f32 v[2:3], v[2:3], v[38:39]
.LBB1_11:
	v_mfma_f32_32x32x16_f16 v[50:65], v[50:53], v[144:147], 0
	s_add_i32 s2, s45, 0x4000
	s_cmpk_lg_u32 s45, 0x8000
	s_cselect_b32 s43, s2, 0
	v_add_u32_e32 v156, s48, v215
	ds_read_b64_tr_b16 v[118:119], v156 offset:49152
	ds_read_b64_tr_b16 v[120:121], v156 offset:49664
	v_add_f32_e32 v38, v66, v67
	v_add_f32_e32 v38, v68, v38
	v_add_f32_e32 v38, v69, v38
	v_add_f32_e32 v38, v70, v38
	v_add_f32_e32 v38, v71, v38
	s_waitcnt lgkmcnt(9)
	v_cvt_pk_f16_f32 v128, v66, v67
	v_cvt_pk_f16_f32 v129, v68, v69
	s_nop 0
	ds_read_b64_tr_b16 v[152:153], v156 offset:53248
	ds_read_b64_tr_b16 v[154:155], v156 offset:53760
	v_add_f32_e32 v66, v72, v38
	s_waitcnt lgkmcnt(10)
	v_mfma_f32_32x32x16_f16 v[34:49], v[34:37], v[144:147], 0
	v_add_f32_e32 v66, v73, v66
	v_add_f32_e32 v66, v74, v66
	v_add_f32_e32 v66, v75, v66
	v_cvt_pk_f16_f32 v130, v70, v71
	v_cvt_pk_f16_f32 v131, v72, v73
	s_nop 0
	ds_read_b64_tr_b16 v[148:149], v156 offset:50176
	ds_read_b64_tr_b16 v[150:151], v156 offset:50688
	s_waitcnt lgkmcnt(11)
	v_mfma_f32_32x32x16_f16 v[50:65], v[122:125], v[140:143], v[50:65]
	v_add_f32_e32 v66, v76, v66
	v_add_f32_e32 v66, v77, v66
	v_add_f32_e32 v66, v78, v66
	v_add_f32_e32 v66, v79, v66
	v_cvt_pk_f16_f32 v106, v74, v75
	v_cvt_pk_f16_f32 v107, v76, v77
	s_nop 0
	ds_read_b64_tr_b16 v[122:123], v156 offset:54272
	ds_read_b64_tr_b16 v[124:125], v156 offset:54784
	s_waitcnt lgkmcnt(12)
	v_mfma_f32_32x32x16_f16 v[34:49], v[172:175], v[140:143], v[34:49]
	v_add_f32_e32 v66, v80, v66
	v_add_f32_e32 v66, v81, v66
	v_add_f32_e32 v66, v82, v66
	v_add_f32_e32 v66, v83, v66
	v_cvt_pk_f16_f32 v108, v78, v79
	v_cvt_pk_f16_f32 v109, v80, v81
	s_nop 0
	ds_read_b64_tr_b16 v[114:115], v156 offset:51200
	ds_read_b64_tr_b16 v[116:117], v156 offset:51712
	s_waitcnt lgkmcnt(13)
	v_mfma_f32_32x32x16_f16 v[50:65], v[176:179], v[136:139], v[50:65]
	v_add_f32_e32 v66, v84, v66
	v_add_f32_e32 v66, v85, v66
	v_add_f32_e32 v66, v86, v66
	v_add_f32_e32 v66, v87, v66
	v_cvt_pk_f16_f32 v102, v82, v83
	v_cvt_pk_f16_f32 v103, v84, v85
	s_nop 0
	ds_read_b64_tr_b16 v[110:111], v156 offset:55296
	ds_read_b64_tr_b16 v[112:113], v156 offset:55808
	s_waitcnt lgkmcnt(14)
	v_mfma_f32_32x32x16_f16 v[34:49], v[164:167], v[136:139], v[34:49]
	v_add_f32_e32 v82, v88, v66
	v_add_f32_e32 v82, v89, v82
	v_add_f32_e32 v82, v90, v82
	v_add_f32_e32 v82, v91, v82
	v_cvt_pk_f16_f32 v104, v86, v87
	v_cvt_pk_f16_f32 v105, v88, v89
	s_nop 0
	ds_read_b64_tr_b16 v[172:173], v156 offset:52224
	ds_read_b64_tr_b16 v[174:175], v156 offset:52736
	s_waitcnt lgkmcnt(14)
	v_mfma_f32_32x32x16_f16 v[50:65], v[168:171], v[132:135], v[50:65]
	v_add_f32_e32 v82, v92, v82
	v_add_f32_e32 v82, v93, v82
	v_add_f32_e32 v82, v94, v82
	v_add_f32_e32 v82, v95, v82
	v_cvt_pk_f16_f32 v98, v90, v91
	v_cvt_pk_f16_f32 v99, v92, v93
	s_nop 0
	ds_read_b64_tr_b16 v[176:177], v156 offset:56320
	ds_read_b64_tr_b16 v[178:179], v156 offset:56832
	v_mfma_f32_32x32x16_f16 v[34:49], v[160:163], v[132:135], v[34:49]
	v_add_f32_e32 v82, v96, v82
	v_add_f32_e32 v82, v97, v82
	v_add_f32_e32 v156, 0, v82
	v_cvt_pk_f16_f32 v100, v94, v95
	v_cvt_pk_f16_f32 v101, v96, v97
	s_nop 0
	s_add_i32 s49, s49, -16
	s_min_i32 s50, s49, s33
	s_cmp_gt_u32 s46, s44
	s_cselect_b64 s[2:3], -1, 0
	s_and_b64 s[48:49], s[2:3], exec
	s_cselect_b32 s48, s50, s46
	s_ashr_i32 s49, s48, 31
	s_lshl_b64 s[48:49], s[48:49], 18
	v_lshl_add_u64 v[82:83], v[194:195], 0, s[48:49]
	s_add_i32 s48, s45, s41
	s_bitcmp1_b32 s54, 8
	s_cbranch_scc1 .Ldmaskip_17
	s_mov_b32 s49, m0
	s_mov_b32 m0, s48
	s_nop 0
	global_load_lds_dwordx4 v[82:83], off
	s_mov_b32 m0, s49
	s_cmp_ge_u32 s48, 0xc000
	s_cselect_b32 s56, 64, 0x10000
	v_lshl_add_u64 v[220:221], v[82:83], 0, s[56:57]
	s_add_i32 s55, s48, 0x1000
	s_mov_b32 m0, s55
	s_nop 0
	global_load_lds_dwordx4 v[220:221], off
.Ldmaskip_17:
	v_lshl_add_u64 v[82:83], v[82:83], 0, s[22:23]
	s_addk_i32 s48, 0x2000
	s_bitcmp1_b32 s54, 8
	s_cbranch_scc1 .Ldmaskip_18
	s_mov_b32 s49, m0
	s_mov_b32 m0, s48
	s_nop 0
	global_load_lds_dwordx4 v[82:83], off
	s_mov_b32 m0, s49
	s_cmp_ge_u32 s48, 0xc000
	s_cselect_b32 s56, 64, 0x10000
	v_lshl_add_u64 v[220:221], v[82:83], 0, s[56:57]
	s_add_i32 s55, s48, 0x1000
	s_mov_b32 m0, s55
	s_nop 0
	global_load_lds_dwordx4 v[220:221], off
.Ldmaskip_18:
	v_lshl_add_u64 v[82:83], v[126:127], 0, s[24:25]
	s_add_i32 s48, s43, s40
	s_bitcmp1_b32 s54, 8
	s_cbranch_scc1 .Ldmaskip_19
	s_mov_b32 s49, m0
	s_mov_b32 m0, s48
	s_nop 0
	global_load_lds_dwordx4 v[82:83], off
	s_mov_b32 m0, s49
	s_cmp_ge_u32 s48, 0xc000
	s_cselect_b32 s56, 64, 0x10000
	v_lshl_add_u64 v[220:221], v[82:83], 0, s[56:57]
	s_add_i32 s55, s48, 0x1000
	s_mov_b32 m0, s55
	s_nop 0
	global_load_lds_dwordx4 v[220:221], off
.Ldmaskip_19:
	v_lshl_add_u64 v[82:83], v[126:127], 0, s[26:27]
	s_addk_i32 s48, 0x2000
	s_bitcmp1_b32 s54, 8
	s_cbranch_scc1 .Ldmaskip_20
	s_mov_b32 s49, m0
	s_mov_b32 m0, s48
	s_nop 0
	global_load_lds_dwordx4 v[82:83], off
	s_mov_b32 m0, s49
	s_cmp_ge_u32 s48, 0xc000
	s_cselect_b32 s56, 64, 0x10000
	v_lshl_add_u64 v[220:221], v[82:83], 0, s[56:57]
	s_add_i32 s55, s48, 0x1000
	s_mov_b32 m0, s55
	s_nop 0
	global_load_lds_dwordx4 v[220:221], off
.Ldmaskip_20:
	s_andn2_b64 vcc, exec, s[30:31]
	s_mov_b64 s[30:31], -1
	s_cbranch_vccz .LBB1_24
	s_andn2_b64 vcc, exec, s[30:31]
	s_cbranch_vccnz .LBB1_15

.LBB1_16:
	s_waitcnt lgkmcnt(14)
	v_mfma_f32_32x32x16_f16 v[18:33], v[128:131], v[118:121], v[18:33]
	v_exp_f32_e32 v50, v50
	v_exp_f32_e32 v51, v51
	v_exp_f32_e32 v52, v52
	v_exp_f32_e32 v53, v53
	s_waitcnt lgkmcnt(12)
	v_mfma_f32_32x32x16_f16 v[2:17], v[128:131], v[152:155], v[2:17]
	v_exp_f32_e32 v54, v54
	v_exp_f32_e32 v55, v55
	v_exp_f32_e32 v56, v56
	v_exp_f32_e32 v57, v57
	v_add_u32_e32 v70, s43, v217
	v_add_u32_e32 v71, v70, v207
	ds_read_b128 v[66:69], v71
	ds_read_b128 v[82:85], v71 offset:4096
	s_waitcnt lgkmcnt(12)
	v_mfma_f32_32x32x16_f16 v[18:33], v[106:109], v[148:151], v[18:33]
	v_exp_f32_e32 v58, v58
	v_exp_f32_e32 v59, v59
	v_exp_f32_e32 v60, v60
	v_exp_f32_e32 v61, v61
	v_add_u32_e32 v71, v70, v206
	ds_read_b128 v[168:171], v71
	ds_read_b128 v[164:167], v71 offset:4096
	s_waitcnt lgkmcnt(12)
	v_mfma_f32_32x32x16_f16 v[2:17], v[106:109], v[122:125], v[2:17]
	v_exp_f32_e32 v62, v62
	v_exp_f32_e32 v63, v63
	v_exp_f32_e32 v64, v64
	v_exp_f32_e32 v65, v65
	v_add_u32_e32 v71, v70, v205
	ds_read_b128 v[160:163], v71
	ds_read_b128 v[156:159], v71 offset:4096
	s_waitcnt lgkmcnt(12)
	v_mfma_f32_32x32x16_f16 v[18:33], v[102:105], v[114:117], v[18:33]
	v_exp_f32_e32 v34, v34
	v_exp_f32_e32 v35, v35
	v_exp_f32_e32 v36, v36
	v_exp_f32_e32 v37, v37
	v_add_u32_e32 v70, v70, v204
	ds_read_b128 v[152:155], v70
	ds_read_b128 v[148:151], v70 offset:4096
	s_waitcnt lgkmcnt(12)
	v_mfma_f32_32x32x16_f16 v[2:17], v[102:105], v[110:113], v[2:17]
	v_exp_f32_e32 v38, v38
	v_exp_f32_e32 v39, v39
	v_exp_f32_e32 v40, v40
	v_exp_f32_e32 v41, v41
	s_waitcnt lgkmcnt(10)
	v_mfma_f32_32x32x16_f16 v[18:33], v[98:101], v[172:175], v[18:33]
	v_exp_f32_e32 v42, v42
	v_exp_f32_e32 v43, v43
	v_exp_f32_e32 v44, v44
	v_exp_f32_e32 v45, v45
	s_waitcnt lgkmcnt(8)
	v_mfma_f32_32x32x16_f16 v[2:17], v[98:101], v[176:179], v[2:17]
	v_exp_f32_e32 v46, v46
	v_exp_f32_e32 v47, v47
	v_exp_f32_e32 v48, v48
	v_exp_f32_e32 v49, v49
	s_waitcnt vmcnt(8) lgkmcnt(0)
	s_barrier
	s_andn2_b64 vcc, exec, s[30:31]
	s_cbranch_vccnz .LBB1_18
	ds_read_b128 v[70:73], v213 offset:96
	ds_read_b128 v[74:77], v213 offset:64
	ds_read_b128 v[78:81], v213 offset:32
	ds_read_b128 v[86:89], v213
	s_waitcnt lgkmcnt(3)
	v_pk_mul_f32 v[32:33], v[32:33], v[72:73]
	s_waitcnt lgkmcnt(2)
	v_pk_mul_f32 v[28:29], v[28:29], v[76:77]
	s_waitcnt lgkmcnt(1)
	v_pk_mul_f32 v[24:25], v[24:25], v[80:81]
	s_waitcnt lgkmcnt(0)
	v_pk_mul_f32 v[20:21], v[20:21], v[88:89]
	v_pk_mul_f32 v[30:31], v[30:31], v[70:71]
	v_pk_mul_f32 v[26:27], v[26:27], v[74:75]
	v_pk_mul_f32 v[22:23], v[22:23], v[78:79]
	v_pk_mul_f32 v[18:19], v[18:19], v[86:87]
	v_pk_mul_f32 v[16:17], v[16:17], v[72:73]
	v_pk_mul_f32 v[12:13], v[12:13], v[76:77]
	v_pk_mul_f32 v[8:9], v[8:9], v[80:81]
	v_pk_mul_f32 v[4:5], v[4:5], v[88:89]
	v_pk_mul_f32 v[14:15], v[14:15], v[70:71]
	v_pk_mul_f32 v[10:11], v[10:11], v[74:75]
	v_pk_mul_f32 v[6:7], v[6:7], v[78:79]
	v_pk_mul_f32 v[2:3], v[2:3], v[86:87]

.LBB1_30:
	s_add_i32 s24, s46, -4
	s_cmp_ge_u32 s24, s44
	s_cbranch_scc1 .LBB1_39
	s_xor_b64 s[2:3], s[20:21], -1
	s_add_i32 s22, s24, 1
	v_add_u32_e32 v126, s45, v215
	ds_read_b64_tr_b16 v[122:123], v126 offset:49152
	ds_read_b64_tr_b16 v[124:125], v126 offset:49664
	v_add_f32_e32 v70, v50, v51
	v_add_f32_e32 v70, v52, v70
	v_add_f32_e32 v70, v53, v70
	v_add_f32_e32 v70, v54, v70
	v_add_f32_e32 v86, v55, v70
	s_waitcnt lgkmcnt(9)
	v_mfma_f32_32x32x16_f16 v[66:81], v[66:69], v[144:147], 0
	v_cvt_pk_f16_f32 v128, v50, v51
	v_cvt_pk_f16_f32 v129, v52, v53
	s_mov_b32 s23, 0
	ds_read_b64_tr_b16 v[184:185], v126 offset:53248
	ds_read_b64_tr_b16 v[186:187], v126 offset:53760
	v_add_f32_e32 v50, v56, v86
	s_waitcnt lgkmcnt(10)
	v_mfma_f32_32x32x16_f16 v[82:97], v[82:85], v[144:147], 0
	v_add_f32_e32 v50, v57, v50
	v_add_f32_e32 v50, v58, v50
	v_add_f32_e32 v50, v59, v50
	v_cvt_pk_f16_f32 v130, v54, v55
	v_cvt_pk_f16_f32 v131, v56, v57
	s_nop 0
	ds_read_b64_tr_b16 v[176:177], v126 offset:50176
	ds_read_b64_tr_b16 v[178:179], v126 offset:50688
	s_waitcnt lgkmcnt(11)
	v_mfma_f32_32x32x16_f16 v[66:81], v[168:171], v[140:143], v[66:81]
	v_add_f32_e32 v50, v60, v50
	v_add_f32_e32 v50, v61, v50
	v_add_f32_e32 v50, v62, v50
	v_add_f32_e32 v50, v63, v50
	v_cvt_pk_f16_f32 v106, v58, v59
	v_cvt_pk_f16_f32 v107, v60, v61
	s_nop 0
	ds_read_b64_tr_b16 v[118:119], v126 offset:54272
	ds_read_b64_tr_b16 v[120:121], v126 offset:54784
	s_waitcnt lgkmcnt(12)
	v_mfma_f32_32x32x16_f16 v[82:97], v[164:167], v[140:143], v[82:97]
	v_add_f32_e32 v50, v64, v50
	v_add_f32_e32 v50, v65, v50
	v_add_f32_e32 v50, v34, v50
	v_add_f32_e32 v50, v35, v50
	v_cvt_pk_f16_f32 v108, v62, v63
	v_cvt_pk_f16_f32 v109, v64, v65
	s_nop 0
	ds_read_b64_tr_b16 v[114:115], v126 offset:51200
	ds_read_b64_tr_b16 v[116:117], v126 offset:51712
	s_waitcnt lgkmcnt(13)
	v_mfma_f32_32x32x16_f16 v[66:81], v[160:163], v[136:139], v[66:81]
	v_add_f32_e32 v50, v36, v50
	v_add_f32_e32 v50, v37, v50
	v_add_f32_e32 v50, v38, v50
	v_add_f32_e32 v50, v39, v50
	v_cvt_pk_f16_f32 v102, v34, v35
	v_cvt_pk_f16_f32 v103, v36, v37
	s_nop 0
	ds_read_b64_tr_b16 v[110:111], v126 offset:55296
	ds_read_b64_tr_b16 v[112:113], v126 offset:55808
	s_waitcnt lgkmcnt(14)
	v_mfma_f32_32x32x16_f16 v[82:97], v[156:159], v[136:139], v[82:97]
	v_add_f32_e32 v34, v40, v50
	v_add_f32_e32 v34, v41, v34
	v_add_f32_e32 v34, v42, v34
	v_add_f32_e32 v34, v43, v34
	v_cvt_pk_f16_f32 v104, v38, v39
	v_cvt_pk_f16_f32 v105, v40, v41
	s_nop 0
	ds_read_b64_tr_b16 v[172:173], v126 offset:52224
	ds_read_b64_tr_b16 v[174:175], v126 offset:52736
	s_waitcnt lgkmcnt(14)
	v_mfma_f32_32x32x16_f16 v[66:81], v[152:155], v[132:135], v[66:81]
	v_add_f32_e32 v34, v44, v34
	v_add_f32_e32 v34, v45, v34
	v_add_f32_e32 v34, v46, v34
	v_add_f32_e32 v34, v47, v34
	v_cvt_pk_f16_f32 v98, v42, v43
	v_cvt_pk_f16_f32 v99, v44, v45
	s_nop 0
	ds_read_b64_tr_b16 v[180:181], v126 offset:56320
	ds_read_b64_tr_b16 v[182:183], v126 offset:56832
	v_mfma_f32_32x32x16_f16 v[82:97], v[148:151], v[132:135], v[82:97]
	v_add_f32_e32 v34, v48, v34
	v_add_f32_e32 v34, v49, v34
	v_add_f32_e32 v126, 0, v34
	v_cvt_pk_f16_f32 v100, v46, v47
	v_cvt_pk_f16_f32 v101, v48, v49
	s_nop 0
	s_add_i32 s24, s33, s24
	s_add_i32 s24, s24, -13
	s_min_i32 s24, s24, s33
	s_ashr_i32 s25, s24, 31
	s_lshl_b64 s[24:25], s[24:25], 18
	v_lshl_add_u64 v[34:35], v[194:195], 0, s[24:25]
	s_add_i32 s26, s43, s41
	s_bitcmp1_b32 s54, 8
	s_cbranch_scc1 .Ldmaskip_21
	s_mov_b32 s24, m0
	s_mov_b32 m0, s26
	s_nop 0
	global_load_lds_dwordx4 v[34:35], off
	s_mov_b32 m0, s24
	s_cmp_ge_u32 s26, 0xc000
	s_cselect_b32 s56, 64, 0x10000
	v_lshl_add_u64 v[220:221], v[34:35], 0, s[56:57]
	s_add_i32 s55, s26, 0x1000
	s_mov_b32 m0, s55
	s_nop 0
	global_load_lds_dwordx4 v[220:221], off
.Ldmaskip_21:
	s_mov_b64 s[24:25], 0x20000
	v_lshl_add_u64 v[34:35], v[34:35], 0, s[24:25]
	s_addk_i32 s26, 0x2000
	s_bitcmp1_b32 s54, 8
	s_cbranch_scc1 .Ldmaskip_22
	s_mov_b32 s27, m0
	s_mov_b32 m0, s26
	s_nop 0
	global_load_lds_dwordx4 v[34:35], off
	s_mov_b32 m0, s27
	s_cmp_ge_u32 s26, 0xc000
	s_cselect_b32 s56, 64, 0x10000
	v_lshl_add_u64 v[220:221], v[34:35], 0, s[56:57]
	s_add_i32 s55, s26, 0x1000
	s_mov_b32 m0, s55
	s_nop 0
	global_load_lds_dwordx4 v[220:221], off
.Ldmaskip_22:
	s_lshl_b64 s[22:23], s[22:23], 18
	v_lshl_add_u64 v[34:35], v[196:197], 0, s[22:23]
	s_add_i32 s22, s30, s40
	s_bitcmp1_b32 s54, 8
	s_cbranch_scc1 .Ldmaskip_23
	s_mov_b32 s23, m0
	s_mov_b32 m0, s22
	s_nop 0
	global_load_lds_dwordx4 v[34:35], off
	s_mov_b32 m0, s23
	s_cmp_ge_u32 s22, 0xc000
	s_cselect_b32 s56, 64, 0x10000
	v_lshl_add_u64 v[220:221], v[34:35], 0, s[56:57]
	s_add_i32 s55, s22, 0x1000
	s_mov_b32 m0, s55
	s_nop 0
	global_load_lds_dwordx4 v[220:221], off
.Ldmaskip_23:
	v_lshl_add_u64 v[34:35], v[34:35], 0, s[24:25]
	s_addk_i32 s22, 0x2000
	s_andn2_b64 vcc, exec, s[2:3]
	s_bitcmp1_b32 s54, 8
	s_cbranch_scc1 .Ldmaskip_24
	s_mov_b32 s2, m0
	s_mov_b32 m0, s22
	s_nop 0
	global_load_lds_dwordx4 v[34:35], off
	s_mov_b32 m0, s2
	s_cmp_ge_u32 s22, 0xc000
	s_cselect_b32 s56, 64, 0x10000
	v_lshl_add_u64 v[220:221], v[34:35], 0, s[56:57]
	s_add_i32 s55, s22, 0x1000
	s_mov_b32 m0, s55
	s_nop 0
	global_load_lds_dwordx4 v[220:221], off
.Ldmaskip_24:
	s_cbranch_vccz .LBB1_120

.LBB1_36:
	s_waitcnt lgkmcnt(14)
	v_mfma_f32_32x32x16_f16 v[18:33], v[128:131], v[122:125], v[18:33]
	v_exp_f32_e32 v50, v50
	v_exp_f32_e32 v51, v51
	v_exp_f32_e32 v52, v52
	v_exp_f32_e32 v53, v53
	s_waitcnt lgkmcnt(12)
	v_mfma_f32_32x32x16_f16 v[2:17], v[128:131], v[184:187], v[2:17]
	v_exp_f32_e32 v54, v54
	v_exp_f32_e32 v55, v55
	v_exp_f32_e32 v56, v56
	v_exp_f32_e32 v57, v57
	v_add_u32_e32 v70, s30, v217
	v_add_u32_e32 v71, v70, v207
	ds_read_b128 v[66:69], v71
	ds_read_b128 v[82:85], v71 offset:4096
	s_waitcnt lgkmcnt(12)
	v_mfma_f32_32x32x16_f16 v[18:33], v[106:109], v[176:179], v[18:33]
	v_exp_f32_e32 v58, v58
	v_exp_f32_e32 v59, v59
	v_exp_f32_e32 v60, v60
	v_exp_f32_e32 v61, v61
	v_add_u32_e32 v71, v70, v206
	ds_read_b128 v[168:171], v71
	ds_read_b128 v[164:167], v71 offset:4096
	s_waitcnt lgkmcnt(12)
	v_mfma_f32_32x32x16_f16 v[2:17], v[106:109], v[118:121], v[2:17]
	v_exp_f32_e32 v62, v62
	v_exp_f32_e32 v63, v63
	v_exp_f32_e32 v64, v64
	v_exp_f32_e32 v65, v65
	v_add_u32_e32 v71, v70, v205
	ds_read_b128 v[160:163], v71
	ds_read_b128 v[156:159], v71 offset:4096
	s_waitcnt lgkmcnt(12)
	v_mfma_f32_32x32x16_f16 v[18:33], v[102:105], v[114:117], v[18:33]
	v_exp_f32_e32 v34, v34
	v_exp_f32_e32 v35, v35
	v_exp_f32_e32 v36, v36
	v_exp_f32_e32 v37, v37
	v_add_u32_e32 v70, v70, v204
	ds_read_b128 v[152:155], v70
	ds_read_b128 v[148:151], v70 offset:4096
	s_waitcnt lgkmcnt(12)
	v_mfma_f32_32x32x16_f16 v[2:17], v[102:105], v[110:113], v[2:17]
	v_exp_f32_e32 v38, v38
	v_exp_f32_e32 v39, v39
	v_exp_f32_e32 v40, v40
	v_exp_f32_e32 v41, v41
	s_waitcnt lgkmcnt(10)
	v_mfma_f32_32x32x16_f16 v[18:33], v[98:101], v[172:175], v[18:33]
	v_exp_f32_e32 v42, v42
	v_exp_f32_e32 v43, v43
	v_exp_f32_e32 v44, v44
	v_exp_f32_e32 v45, v45
	s_waitcnt lgkmcnt(8)
	v_mfma_f32_32x32x16_f16 v[2:17], v[98:101], v[180:183], v[2:17]
	v_exp_f32_e32 v46, v46
	v_exp_f32_e32 v47, v47
	v_exp_f32_e32 v48, v48
	v_exp_f32_e32 v49, v49
	s_waitcnt vmcnt(8) lgkmcnt(0)
	s_barrier
	s_andn2_b64 vcc, exec, s[2:3]
	s_cbranch_vccnz .LBB1_38
	ds_read_b128 v[70:73], v213 offset:96
	ds_read_b128 v[74:77], v213 offset:64
	ds_read_b128 v[78:81], v213 offset:32
	ds_read_b128 v[86:89], v213
	s_waitcnt lgkmcnt(3)
	v_pk_mul_f32 v[32:33], v[32:33], v[72:73]
	s_waitcnt lgkmcnt(2)
	v_pk_mul_f32 v[28:29], v[28:29], v[76:77]
	s_waitcnt lgkmcnt(1)
	v_pk_mul_f32 v[24:25], v[24:25], v[80:81]
	s_waitcnt lgkmcnt(0)
	v_pk_mul_f32 v[20:21], v[20:21], v[88:89]
	v_pk_mul_f32 v[30:31], v[30:31], v[70:71]
	v_pk_mul_f32 v[26:27], v[26:27], v[74:75]
	v_pk_mul_f32 v[22:23], v[22:23], v[78:79]
	v_pk_mul_f32 v[18:19], v[18:19], v[86:87]
	v_pk_mul_f32 v[16:17], v[16:17], v[72:73]
	v_pk_mul_f32 v[12:13], v[12:13], v[76:77]
	v_pk_mul_f32 v[8:9], v[8:9], v[80:81]
	v_pk_mul_f32 v[4:5], v[4:5], v[88:89]
	v_pk_mul_f32 v[14:15], v[14:15], v[70:71]
	v_pk_mul_f32 v[10:11], v[10:11], v[74:75]
	v_pk_mul_f32 v[6:7], v[6:7], v[78:79]
	v_pk_mul_f32 v[2:3], v[2:3], v[86:87]

.LBB1_39:
	s_lshl_b32 s2, s33, 7
	s_or_b32 s2, s39, s2
	s_or_b32 s18, s18, s2
	s_lshl_b64 s[2:3], s[18:19], 11
	s_add_u32 s2, s4, s2
	s_addc_u32 s3, s5, s3
	s_lshl_b32 s22, s42, 1
	s_add_u32 s2, s2, s22
	s_addc_u32 s3, s3, 0
	global_load_dwordx4 v[124:127], v216, s[2:3]
	global_load_dwordx4 v[120:123], v216, s[2:3] offset:32
	global_load_dwordx4 v[116:119], v216, s[2:3] offset:64
	global_load_dwordx4 v[112:115], v216, s[2:3] offset:96
	s_mov_b32 s3, 0
	v_add_u32_e32 v110, s45, v215
	ds_read_b64_tr_b16 v[172:173], v110 offset:49152
	ds_read_b64_tr_b16 v[174:175], v110 offset:49664
	v_add_f32_e32 v70, v50, v51
	v_add_f32_e32 v70, v52, v70
	v_add_f32_e32 v70, v53, v70
	v_add_f32_e32 v70, v54, v70
	v_add_f32_e32 v86, v55, v70
	s_waitcnt lgkmcnt(9)
	v_mfma_f32_32x32x16_f16 v[66:81], v[66:69], v[144:147], 0
	v_cvt_pk_f16_f32 v128, v50, v51
	v_cvt_pk_f16_f32 v129, v52, v53
	s_nop 0
	ds_read_b64_tr_b16 v[176:177], v110 offset:53248
	ds_read_b64_tr_b16 v[178:179], v110 offset:53760
	v_add_f32_e32 v50, v56, v86
	s_waitcnt lgkmcnt(10)
	v_mfma_f32_32x32x16_f16 v[82:97], v[82:85], v[144:147], 0
	v_add_f32_e32 v50, v57, v50
	v_add_f32_e32 v50, v58, v50
	v_add_f32_e32 v50, v59, v50
	v_cvt_pk_f16_f32 v130, v54, v55
	v_cvt_pk_f16_f32 v131, v56, v57
	s_nop 0
	ds_read_b64_tr_b16 v[144:145], v110 offset:50176
	ds_read_b64_tr_b16 v[146:147], v110 offset:50688
	s_waitcnt lgkmcnt(11)
	v_mfma_f32_32x32x16_f16 v[66:81], v[168:171], v[140:143], v[66:81]
	v_add_f32_e32 v50, v60, v50
	v_add_f32_e32 v50, v61, v50
	v_add_f32_e32 v50, v62, v50
	v_add_f32_e32 v50, v63, v50
	v_cvt_pk_f16_f32 v106, v58, v59
	v_cvt_pk_f16_f32 v107, v60, v61
	s_nop 0
	ds_read_b64_tr_b16 v[168:169], v110 offset:54272
	ds_read_b64_tr_b16 v[170:171], v110 offset:54784
	s_waitcnt lgkmcnt(12)
	v_mfma_f32_32x32x16_f16 v[82:97], v[164:167], v[140:143], v[82:97]
	v_add_f32_e32 v50, v64, v50
	v_add_f32_e32 v50, v65, v50
	v_add_f32_e32 v50, v34, v50
	v_add_f32_e32 v50, v35, v50
	v_cvt_pk_f16_f32 v108, v62, v63
	v_cvt_pk_f16_f32 v109, v64, v65
	s_nop 0
	ds_read_b64_tr_b16 v[140:141], v110 offset:51200
	ds_read_b64_tr_b16 v[142:143], v110 offset:51712
	s_waitcnt lgkmcnt(13)
	v_mfma_f32_32x32x16_f16 v[66:81], v[160:163], v[136:139], v[66:81]
	v_add_f32_e32 v50, v36, v50
	v_add_f32_e32 v50, v37, v50
	v_add_f32_e32 v50, v38, v50
	v_add_f32_e32 v50, v39, v50
	v_cvt_pk_f16_f32 v102, v34, v35
	v_cvt_pk_f16_f32 v103, v36, v37
	s_nop 0
	ds_read_b64_tr_b16 v[160:161], v110 offset:55296
	ds_read_b64_tr_b16 v[162:163], v110 offset:55808
	s_waitcnt lgkmcnt(14)
	v_mfma_f32_32x32x16_f16 v[82:97], v[156:159], v[136:139], v[82:97]
	v_add_f32_e32 v34, v40, v50
	v_add_f32_e32 v34, v41, v34
	v_add_f32_e32 v34, v42, v34
	v_add_f32_e32 v34, v43, v34
	v_cvt_pk_f16_f32 v104, v38, v39
	v_cvt_pk_f16_f32 v105, v40, v41
	s_nop 0
	ds_read_b64_tr_b16 v[136:137], v110 offset:52224
	ds_read_b64_tr_b16 v[138:139], v110 offset:52736
	s_waitcnt lgkmcnt(14)
	v_mfma_f32_32x32x16_f16 v[66:81], v[152:155], v[132:135], v[66:81]
	v_add_f32_e32 v34, v44, v34
	v_add_f32_e32 v34, v45, v34
	v_add_f32_e32 v34, v46, v34
	v_add_f32_e32 v34, v47, v34
	v_cvt_pk_f16_f32 v98, v42, v43
	v_cvt_pk_f16_f32 v99, v44, v45
	s_nop 0
	ds_read_b64_tr_b16 v[152:153], v110 offset:56320
	ds_read_b64_tr_b16 v[154:155], v110 offset:56832
	v_mfma_f32_32x32x16_f16 v[82:97], v[148:151], v[132:135], v[82:97]
	v_add_f32_e32 v34, v48, v34
	v_add_f32_e32 v34, v49, v34
	v_add_f32_e32 v34, 0, v34
	v_cvt_pk_f16_f32 v100, v46, v47
	v_cvt_pk_f16_f32 v101, v48, v49
	s_nop 0
	s_min_u32 s2, s33, 2
	s_lshl_b32 s2, s2, 18
	v_lshl_add_u64 v[36:37], v[194:195], 0, s[2:3]
	s_add_i32 s4, s43, s41
	s_bitcmp1_b32 s54, 8
	s_cbranch_scc1 .Ldmaskip_25
	s_mov_b32 s2, m0
	s_mov_b32 m0, s4
	s_nop 0
	global_load_lds_dwordx4 v[36:37], off
	s_mov_b32 m0, s2
	s_cmp_ge_u32 s4, 0xc000
	s_cselect_b32 s56, 64, 0x10000
	v_lshl_add_u64 v[220:221], v[36:37], 0, s[56:57]
	s_add_i32 s55, s4, 0x1000
	s_mov_b32 m0, s55
	s_nop 0
	global_load_lds_dwordx4 v[220:221], off
.Ldmaskip_25:
	s_mov_b64 s[2:3], 0x20000
	v_lshl_add_u64 v[36:37], v[36:37], 0, s[2:3]
	s_add_i32 s2, s4, 0x2000
	s_bitcmp1_b32 s54, 8
	s_cbranch_scc1 .Ldmaskip_26
	s_mov_b32 s3, m0
	s_mov_b32 m0, s2
	s_nop 0
	global_load_lds_dwordx4 v[36:37], off
	s_mov_b32 m0, s3
	s_cmp_ge_u32 s2, 0xc000
	s_cselect_b32 s56, 64, 0x10000
	v_lshl_add_u64 v[220:221], v[36:37], 0, s[56:57]
	s_add_i32 s55, s2, 0x1000
	s_mov_b32 m0, s55
	s_nop 0
	global_load_lds_dwordx4 v[220:221], off
.Ldmaskip_26:
	s_add_i32 s2, s30, s40
	s_bitcmp1_b32 s54, 8
	s_cbranch_scc1 .Ldmaskip_27
	s_mov_b32 s3, m0
	s_mov_b32 m0, s2
	s_nop 0
	global_load_lds_dwordx4 v[196:197], off
	s_mov_b32 m0, s3
	s_cmp_ge_u32 s2, 0xc000
	s_cselect_b32 s56, 64, 0x10000
	v_lshl_add_u64 v[220:221], v[196:197], 0, s[56:57]
	s_add_i32 s55, s2, 0x1000
	s_mov_b32 m0, s55
	s_nop 0
	global_load_lds_dwordx4 v[220:221], off
.Ldmaskip_27:
	s_addk_i32 s2, 0x2000
	s_bitcmp1_b32 s54, 8
	s_cbranch_scc1 .Ldmaskip_28
	s_mov_b32 s3, m0
	s_mov_b32 m0, s2
	s_nop 0
	global_load_lds_dwordx4 v[198:199], off
	s_mov_b32 m0, s3
	s_cmp_ge_u32 s2, 0xc000
	s_cselect_b32 s56, 64, 0x10000
	v_lshl_add_u64 v[220:221], v[198:199], 0, s[56:57]
	s_add_i32 s55, s2, 0x1000
	s_mov_b32 m0, s55
	s_nop 0
	global_load_lds_dwordx4 v[220:221], off
.Ldmaskip_28:
	s_and_b64 vcc, exec, s[20:21]
	s_cbranch_vccz .LBB1_115

.LBB1_46:
	s_waitcnt vmcnt(8) lgkmcnt(0)
	s_barrier
	v_add_f32_e32 v66, v50, v51
	v_add_u32_e32 v76, s43, v215
	v_add_f32_e32 v66, v52, v66
	ds_read_b64_tr_b16 v[68:69], v76 offset:49152
	ds_read_b64_tr_b16 v[70:71], v76 offset:49664
	v_add_f32_e32 v66, v53, v66
	v_add_f32_e32 v66, v54, v66
	v_add_f32_e32 v66, v55, v66
	v_add_f32_e32 v66, v56, v66
	v_add_f32_e32 v66, v57, v66
	v_cvt_pk_f16_f32 v50, v50, v51
	v_cvt_pk_f16_f32 v51, v52, v53
	v_cvt_pk_f16_f32 v52, v54, v55
	v_cvt_pk_f16_f32 v53, v56, v57
	ds_read_b64_tr_b16 v[54:55], v76 offset:50176
	ds_read_b64_tr_b16 v[56:57], v76 offset:50688
	s_waitcnt lgkmcnt(2)
	v_mfma_f32_32x32x16_f16 v[18:33], v[50:53], v[68:71], v[18:33]
	ds_read_b64_tr_b16 v[68:69], v76 offset:53248
	ds_read_b64_tr_b16 v[70:71], v76 offset:53760
	v_add_f32_e32 v66, v58, v66
	v_add_f32_e32 v66, v59, v66
	v_add_f32_e32 v66, v60, v66
	ds_read_b64_tr_b16 v[72:73], v76 offset:54272
	ds_read_b64_tr_b16 v[74:75], v76 offset:54784
	s_lshl_b32 s2, s38, 13
	s_add_i32 s4, s2, 0
	s_waitcnt lgkmcnt(2)
	v_mfma_f32_32x32x16_f16 v[2:17], v[50:53], v[68:71], v[2:17]
	v_add_f32_e32 v50, v61, v66
	v_add_f32_e32 v50, v62, v50
	v_add_f32_e32 v66, v63, v50
	v_cvt_pk_f16_f32 v50, v58, v59
	v_cvt_pk_f16_f32 v51, v60, v61
	v_cvt_pk_f16_f32 v52, v62, v63
	v_cvt_pk_f16_f32 v53, v64, v65
	s_add_i32 s4, s4, 0x18800
	v_mfma_f32_32x32x16_f16 v[18:33], v[50:53], v[54:57], v[18:33]
	v_add_f32_e32 v54, v64, v66
	v_add_f32_e32 v54, v65, v54
	v_add_f32_e32 v54, v34, v54
	v_add_f32_e32 v54, v35, v54
	v_add_f32_e32 v54, v36, v54
	v_add_f32_e32 v58, v37, v54
	v_cvt_pk_f16_f32 v34, v34, v35
	s_waitcnt lgkmcnt(0)
	v_mfma_f32_32x32x16_f16 v[2:17], v[50:53], v[72:75], v[2:17]
	ds_read_b64_tr_b16 v[50:51], v76 offset:51200
	ds_read_b64_tr_b16 v[52:53], v76 offset:51712
	v_cvt_pk_f16_f32 v35, v36, v37
	v_cvt_pk_f16_f32 v36, v38, v39
	v_cvt_pk_f16_f32 v37, v40, v41
	ds_read_b64_tr_b16 v[54:55], v76 offset:52224
	ds_read_b64_tr_b16 v[56:57], v76 offset:52736
	v_add_f32_e32 v38, v38, v58
	v_add_f32_e32 v38, v39, v38
	s_waitcnt lgkmcnt(2)
	v_mfma_f32_32x32x16_f16 v[18:33], v[34:37], v[50:53], v[18:33]
	ds_read_b64_tr_b16 v[50:51], v76 offset:55296
	ds_read_b64_tr_b16 v[52:53], v76 offset:55808
	v_add_f32_e32 v38, v40, v38
	ds_read_b64_tr_b16 v[58:59], v76 offset:56320
	ds_read_b64_tr_b16 v[60:61], v76 offset:56832
	s_cmp_lg_u32 s37, 1
	v_lshlrev_b32_e32 v196, 4, v212
	s_waitcnt lgkmcnt(2)
	v_mfma_f32_32x32x16_f16 v[2:17], v[34:37], v[50:53], v[2:17]
	v_add_f32_e32 v34, v41, v38
	v_add_f32_e32 v34, v42, v34
	v_add_f32_e32 v38, v43, v34
	v_add_f32_e32 v38, v44, v38
	v_add_f32_e32 v38, v45, v38
	v_cvt_pk_f16_f32 v34, v42, v43
	v_cvt_pk_f16_f32 v35, v44, v45
	v_cvt_pk_f16_f32 v36, v46, v47
	v_cvt_pk_f16_f32 v37, v48, v49
	v_add_f32_e32 v38, v46, v38
	v_mfma_f32_32x32x16_f16 v[18:33], v[34:37], v[54:57], v[18:33]
	v_add_f32_e32 v38, v47, v38
	v_add_f32_e32 v38, v48, v38
	v_add_f32_e32 v38, v49, v38
	v_add_f32_e32 v38, v67, v38
	s_waitcnt lgkmcnt(0)
	v_mfma_f32_32x32x16_f16 v[2:17], v[34:37], v[58:61], v[2:17]
	v_mov_b32_e32 v34, v38
	s_nop 1
	v_permlane32_swap_b32_e32 v38, v34
	v_add_f32_e32 v34, v38, v34
	s_cbranch_scc1 .LBB1_50
	s_and_saveexec_b64 s[2:3], s[0:1]
	ds_write2_b32 v214, v192, v34 offset1:32
	s_or_b64 exec, exec, s[2:3]
	v_add_u32_e32 v35, s4, v196
	ds_write_b128 v35, v[18:21]
	ds_write_b128 v35, v[22:25] offset:1024
	ds_write_b128 v35, v[26:29] offset:2048
	ds_write_b128 v35, v[30:33] offset:3072
	ds_write_b128 v35, v[2:5] offset:4096
	ds_write_b128 v35, v[6:9] offset:5120
	ds_write_b128 v35, v[10:13] offset:6144
	ds_write_b128 v35, v[14:17] offset:7168

.Lu2w_done:
	s_barrier
	s_lshr_b32 s26, s23, 6
	s_mov_b32 s5, 0
	s_add_i32 s27, s27, 0x18000
	v_mov_b32_e32 v15, 0
	v_cmp_neq_f32_e64 s[2:3], 0, v192
	s_andn2_b64 vcc, exec, s[16:17]
	s_mov_b32 s18, 1
	s_cbranch_vccnz .LBB1_86
	s_cmp_eq_u64 s[2:3], 0
	s_cselect_b64 s[2:3], -1, 0
	s_lshl_b32 s4, s26, 2
	s_and_b32 s4, s4, 4
	s_lshl_b32 s19, s25, 14
	s_lshl_b32 s29, s26, 10
	s_cmp_lg_u32 0, -1
	v_bitop3_b32 v0, s4, v200, v208 bitop3:0x36
	s_cselect_b32 s4, 0, 0
	v_lshl_or_b32 v48, s26, 3, v193
	v_mov_b32_e32 v49, 0
	v_or_b32_e32 v4, s19, v1
	s_add_i32 s29, s29, s4
	v_lshlrev_b64 v[2:3], 11, v[48:49]
	s_add_i32 s16, s30, 0x4000
	v_lshlrev_b32_e32 v48, 1, v4
	s_lshl_b32 s4, s24, 6
	s_add_i32 s31, s29, 0xc000
	v_lshl_add_u64 v[4:5], s[14:15], 0, v[48:49]
	s_cmpk_lg_u32 s30, 0x8000
	v_lshl_add_u64 v[2:3], s[6:7], 0, v[2:3]
	v_lshl_add_u64 v[4:5], v[4:5], 0, s[4:5]
	v_lshlrev_b32_e32 v48, 4, v0
	s_cselect_b32 s35, s16, 0
	s_min_u32 s4, s33, 3
	v_lshl_add_u64 v[194:195], v[2:3], 0, v[48:49]
	s_lshl_b32 s4, s4, 18
	v_lshl_add_u64 v[2:3], v[194:195], 0, s[4:5]
	s_add_i32 s4, s29, s30
	s_bitcmp1_b32 s54, 8
	s_cbranch_scc1 .Ldmaskip_29
	s_mov_b32 s6, m0
	s_mov_b32 m0, s4
	s_nop 0
	global_load_lds_dwordx4 v[2:3], off
	s_mov_b32 m0, s6
	s_cmp_ge_u32 s4, 0xc000
	s_cselect_b32 s56, 64, 0x10000
	v_lshl_add_u64 v[220:221], v[2:3], 0, s[56:57]
	s_add_i32 s55, s4, 0x1000
	s_mov_b32 m0, s55
	s_nop 0
	global_load_lds_dwordx4 v[220:221], off
.Ldmaskip_29:
	s_mov_b64 s[6:7], 0x20000
	v_mov_b32_e32 v191, v49
	v_lshl_add_u64 v[2:3], v[2:3], 0, s[6:7]
	s_addk_i32 s4, 0x2000
	s_bitcmp1_b32 s54, 8
	s_cbranch_scc1 .Ldmaskip_30
	s_mov_b32 s14, m0
	s_mov_b32 m0, s4
	s_nop 0
	global_load_lds_dwordx4 v[2:3], off
	s_mov_b32 m0, s14
	s_cmp_ge_u32 s4, 0xc000
	s_cselect_b32 s56, 64, 0x10000
	v_lshl_add_u64 v[220:221], v[2:3], 0, s[56:57]
	s_add_i32 s55, s4, 0x1000
	s_mov_b32 m0, s55
	s_nop 0
	global_load_lds_dwordx4 v[220:221], off
.Ldmaskip_30:
	v_lshl_add_u64 v[190:191], v[4:5], 0, v[190:191]
	s_mov_b64 s[14:15], 0x40000
	v_lshl_add_u64 v[2:3], v[190:191], 0, s[14:15]
	s_add_i32 s4, s31, s35
	s_bitcmp1_b32 s54, 8
	s_cbranch_scc1 .Ldmaskip_31
	s_mov_b32 s16, m0
	s_mov_b32 m0, s4
	s_nop 0
	global_load_lds_dwordx4 v[2:3], off
	s_mov_b32 m0, s16
	s_cmp_ge_u32 s4, 0xc000
	s_cselect_b32 s56, 64, 0x10000
	v_lshl_add_u64 v[220:221], v[2:3], 0, s[56:57]
	s_add_i32 s55, s4, 0x1000
	s_mov_b32 m0, s55
	s_nop 0
	global_load_lds_dwordx4 v[220:221], off
.Ldmaskip_31:
	s_mov_b64 s[16:17], 0x60000
	v_lshl_add_u64 v[2:3], v[190:191], 0, s[16:17]
	v_add_u32_e32 v0, s35, v199
	s_addk_i32 s4, 0x2000
	s_bitcmp1_b32 s54, 8
	s_cbranch_scc1 .Ldmaskip_32
	s_mov_b32 s20, m0
	s_mov_b32 m0, s4
	s_nop 0
	global_load_lds_dwordx4 v[2:3], off
	s_mov_b32 m0, s20
	s_cmp_ge_u32 s4, 0xc000
	s_cselect_b32 s56, 64, 0x10000
	v_lshl_add_u64 v[220:221], v[2:3], 0, s[56:57]
	s_add_i32 s55, s4, 0x1000
	s_mov_b32 m0, s55
	s_nop 0
	global_load_lds_dwordx4 v[220:221], off
.Ldmaskip_32:
	v_add_u32_e32 v2, v0, v207
	ds_read_b128 v[80:83], v2
	ds_read_b128 v[96:99], v2 offset:4096
	v_add_u32_e32 v2, v0, v206
	ds_read_b128 v[164:167], v2
	ds_read_b128 v[160:163], v2 offset:4096
	v_add_u32_e32 v2, v0, v205
	v_add_u32_e32 v0, v0, v204
	ds_read_b128 v[156:159], v2
	ds_read_b128 v[152:155], v2 offset:4096
	ds_read_b128 v[148:151], v0
	ds_read_b128 v[144:147], v0 offset:4096
	s_add_i32 s4, s35, 0x4000
	s_waitcnt vmcnt(8) lgkmcnt(0)
	s_barrier
	s_cmpk_lg_u32 s35, 0x8000
	s_cselect_b32 s28, s4, 0
	s_cmp_lt_u32 s33, 3
	s_cbranch_scc1 .LBB1_87
	s_lshr_b32 s4, s23, 2
	s_and_b32 s4, s4, 0x3fffffc0
	s_add_u32 s20, s12, s4
	s_addc_u32 s21, s13, 0
	v_lshl_add_u64 v[2:3], s[20:21], 0, v[188:189]
	v_add_lshl_u32 v48, s19, v1, 1
	s_add_u32 s8, s8, s34
	v_lshl_add_u64 v[0:1], v[2:3], 0, v[48:49]
	s_addc_u32 s9, s9, 0
	v_lshl_add_u64 v[0:1], s[8:9], 0, v[0:1]
	s_mov_b64 s[8:9], 0x80000
	v_mov_b32_e32 v48, v49
	v_lshl_add_u64 v[180:181], v[0:1], 0, s[8:9]
	v_mov_b32_e32 v50, v49
	v_mov_b32_e32 v51, v49
	v_mov_b32_e32 v52, v49
	v_mov_b32_e32 v53, v49
	v_mov_b32_e32 v54, v49
	v_mov_b32_e32 v55, v49
	v_mov_b32_e32 v56, v49
	v_mov_b32_e32 v57, v49
	v_mov_b32_e32 v58, v49
	v_mov_b32_e32 v59, v49
	v_mov_b32_e32 v60, v49
	v_mov_b32_e32 v61, v49
	v_mov_b32_e32 v62, v49
	v_mov_b32_e32 v63, v49
	v_mov_b64_e32 v[16:17], v[48:49]
	v_mov_b64_e32 v[0:1], v[48:49]
	v_lshl_add_u32 v182, v202, 2, s27
	v_lshl_add_u32 v183, v203, 2, s27
	s_mov_b32 s36, 5
	s_mov_b32 s34, 0x41000000
	v_mov_b32_e32 v184, 0xff800000
	v_mov_b64_e32 v[18:19], v[50:51]
	v_mov_b64_e32 v[20:21], v[52:53]
	v_mov_b64_e32 v[22:23], v[54:55]
	v_mov_b64_e32 v[24:25], v[56:57]
	v_mov_b64_e32 v[26:27], v[58:59]
	v_mov_b64_e32 v[28:29], v[60:61]
	v_mov_b64_e32 v[30:31], v[62:63]
	v_mov_b64_e32 v[2:3], v[50:51]
	v_mov_b64_e32 v[4:5], v[52:53]
	v_mov_b64_e32 v[6:7], v[54:55]
	v_mov_b64_e32 v[8:9], v[56:57]
	v_mov_b64_e32 v[10:11], v[58:59]
	v_mov_b64_e32 v[12:13], v[60:61]
	v_mov_b64_e32 v[14:15], v[62:63]
.LBB1_60:
	v_add_u32_e32 v48, s30, v197
	ds_read_b64_tr_b16 v[172:173], v48 offset:49152
	ds_read_b64_tr_b16 v[174:175], v48 offset:49664
	s_waitcnt lgkmcnt(9)
	v_mfma_f32_32x32x16_f16 v[80:95], v[80:83], v[124:127], 0
	v_add_f32_e32 v50, v64, v65
	v_add_f32_e32 v50, v66, v50
	v_add_f32_e32 v50, v67, v50
	v_add_f32_e32 v50, v68, v50
	v_add_f32_e32 v50, v69, v50
	v_cvt_pk_f16_f32 v140, v64, v65
	v_cvt_pk_f16_f32 v141, v66, v67
	s_nop 0
	ds_read_b64_tr_b16 v[176:177], v48 offset:53248
	ds_read_b64_tr_b16 v[178:179], v48 offset:53760
	s_waitcnt lgkmcnt(10)
	v_mfma_f32_32x32x16_f16 v[96:111], v[96:99], v[124:127], 0
	v_add_f32_e32 v50, v70, v50
	v_add_f32_e32 v50, v71, v50
	v_add_f32_e32 v50, v72, v50
	v_add_f32_e32 v50, v73, v50
	v_cvt_pk_f16_f32 v142, v68, v69
	v_cvt_pk_f16_f32 v143, v70, v71
	s_nop 0
	ds_read_b64_tr_b16 v[168:169], v48 offset:50176
	ds_read_b64_tr_b16 v[170:171], v48 offset:50688
	s_waitcnt lgkmcnt(11)
	v_mfma_f32_32x32x16_f16 v[80:95], v[164:167], v[120:123], v[80:95]
	v_add_f32_e32 v50, v74, v50
	v_add_f32_e32 v50, v75, v50
	v_add_f32_e32 v50, v76, v50
	v_add_f32_e32 v50, v77, v50
	v_cvt_pk_f16_f32 v136, v72, v73
	v_cvt_pk_f16_f32 v137, v74, v75
	s_nop 0
	ds_read_b64_tr_b16 v[164:165], v48 offset:54272
	ds_read_b64_tr_b16 v[166:167], v48 offset:54784
	s_waitcnt lgkmcnt(12)
	v_mfma_f32_32x32x16_f16 v[96:111], v[160:163], v[120:123], v[96:111]
	v_add_f32_e32 v50, v78, v50
	v_add_f32_e32 v50, v79, v50
	v_add_f32_e32 v50, v32, v50
	v_add_f32_e32 v50, v33, v50
	v_cvt_pk_f16_f32 v138, v76, v77
	v_cvt_pk_f16_f32 v139, v78, v79
	s_nop 0
	ds_read_b64_tr_b16 v[70:71], v48 offset:51200
	ds_read_b64_tr_b16 v[72:73], v48 offset:51712
	s_waitcnt lgkmcnt(13)
	v_mfma_f32_32x32x16_f16 v[80:95], v[156:159], v[116:119], v[80:95]
	v_add_f32_e32 v50, v34, v50
	v_add_f32_e32 v50, v35, v50
	v_add_f32_e32 v50, v36, v50
	v_add_f32_e32 v50, v37, v50
	v_cvt_pk_f16_f32 v132, v32, v33
	v_cvt_pk_f16_f32 v133, v34, v35
	s_nop 0
	ds_read_b64_tr_b16 v[66:67], v48 offset:55296
	ds_read_b64_tr_b16 v[68:69], v48 offset:55808
	s_waitcnt lgkmcnt(14)
	v_mfma_f32_32x32x16_f16 v[96:111], v[152:155], v[116:119], v[96:111]
	v_add_f32_e32 v32, v38, v50
	v_add_f32_e32 v32, v39, v32
	v_add_f32_e32 v32, v40, v32
	v_add_f32_e32 v32, v41, v32
	v_cvt_pk_f16_f32 v134, v36, v37
	v_cvt_pk_f16_f32 v135, v38, v39
	s_nop 0
	ds_read_b64_tr_b16 v[74:75], v48 offset:52224
	ds_read_b64_tr_b16 v[76:77], v48 offset:52736
	s_waitcnt lgkmcnt(14)
	v_mfma_f32_32x32x16_f16 v[80:95], v[148:151], v[112:115], v[80:95]
	v_add_f32_e32 v32, v42, v32
	v_add_f32_e32 v32, v43, v32
	v_add_f32_e32 v32, v44, v32
	v_add_f32_e32 v32, v45, v32
	v_cvt_pk_f16_f32 v128, v40, v41
	v_cvt_pk_f16_f32 v129, v42, v43
	s_nop 0
	ds_read_b64_tr_b16 v[148:149], v48 offset:56320
	ds_read_b64_tr_b16 v[150:151], v48 offset:56832
	v_mfma_f32_32x32x16_f16 v[96:111], v[144:147], v[112:115], v[96:111]
	v_add_f32_e32 v32, v46, v32
	v_add_f32_e32 v32, v47, v32
	v_add_f32_e32 v48, 0, v32
	v_cvt_pk_f16_f32 v130, v44, v45
	v_cvt_pk_f16_f32 v131, v46, v47
	s_nop 0
	s_add_i32 s4, s36, -1
	s_min_u32 s4, s4, s33
	s_lshl_b32 s4, s4, 18
	v_lshl_add_u64 v[32:33], v[194:195], 0, s[4:5]
	s_add_i32 s4, s35, s29
	s_bitcmp1_b32 s54, 8
	s_cbranch_scc1 .Ldmaskip_33
	s_mov_b32 s18, m0
	s_mov_b32 m0, s4
	s_nop 0
	global_load_lds_dwordx4 v[32:33], off
	s_mov_b32 m0, s18
	s_cmp_ge_u32 s4, 0xc000
	s_cselect_b32 s56, 64, 0x10000
	v_lshl_add_u64 v[220:221], v[32:33], 0, s[56:57]
	s_add_i32 s55, s4, 0x1000
	s_mov_b32 m0, s55
	s_nop 0
	global_load_lds_dwordx4 v[220:221], off
.Ldmaskip_33:
	v_lshl_add_u64 v[32:33], v[32:33], 0, s[6:7]
	s_addk_i32 s4, 0x2000
	s_bitcmp1_b32 s54, 8
	s_cbranch_scc1 .Ldmaskip_34
	s_mov_b32 s18, m0
	s_mov_b32 m0, s4
	s_nop 0
	global_load_lds_dwordx4 v[32:33], off
	s_mov_b32 m0, s18
	s_cmp_ge_u32 s4, 0xc000
	s_cselect_b32 s56, 64, 0x10000
	v_lshl_add_u64 v[220:221], v[32:33], 0, s[56:57]
	s_add_i32 s55, s4, 0x1000
	s_mov_b32 m0, s55
	s_nop 0
	global_load_lds_dwordx4 v[220:221], off
.Ldmaskip_34:
	s_add_i32 s4, s28, s31
	s_bitcmp1_b32 s54, 8
	s_cbranch_scc1 .Ldmaskip_35
	s_mov_b32 s18, m0
	s_mov_b32 m0, s4
	s_nop 0
	global_load_lds_dwordx4 v[180:181], off
	s_mov_b32 m0, s18
	s_cmp_ge_u32 s4, 0xc000
	s_cselect_b32 s56, 64, 0x10000
	v_lshl_add_u64 v[220:221], v[180:181], 0, s[56:57]
	s_add_i32 s55, s4, 0x1000
	s_mov_b32 m0, s55
	s_nop 0
	global_load_lds_dwordx4 v[220:221], off
.Ldmaskip_35:
	v_lshl_add_u64 v[32:33], v[180:181], 0, s[6:7]
	s_addk_i32 s4, 0x2000
	s_bitcmp1_b32 s54, 8
	s_cbranch_scc1 .Ldmaskip_36
	s_mov_b32 s18, m0
	s_mov_b32 m0, s4
	s_nop 0
	global_load_lds_dwordx4 v[32:33], off
	s_mov_b32 m0, s18
	s_cmp_ge_u32 s4, 0xc000
	s_cselect_b32 s56, 64, 0x10000
	v_lshl_add_u64 v[220:221], v[32:33], 0, s[56:57]
	s_add_i32 s55, s4, 0x1000
	s_mov_b32 m0, s55
	s_nop 0
	global_load_lds_dwordx4 v[220:221], off
.Ldmaskip_36:
	s_and_b64 vcc, exec, s[2:3]
	s_mov_b64 s[18:19], -1
	s_cbranch_vccz .LBB1_76
	s_andn2_b64 vcc, exec, s[18:19]
	s_cbranch_vccnz .LBB1_64

.LBB1_65:
	s_xor_b64 s[18:19], s[2:3], -1
	s_waitcnt lgkmcnt(14)
	v_mfma_f32_32x32x16_f16 v[16:31], v[140:143], v[172:175], v[16:31]
	v_exp_f32_e32 v50, v50
	v_exp_f32_e32 v51, v51
	v_exp_f32_e32 v52, v52
	v_exp_f32_e32 v53, v53
	s_waitcnt lgkmcnt(12)
	v_mfma_f32_32x32x16_f16 v[0:15], v[140:143], v[176:179], v[0:15]
	v_exp_f32_e32 v54, v54
	v_exp_f32_e32 v55, v55
	v_exp_f32_e32 v56, v56
	v_exp_f32_e32 v57, v57
	v_add_u32_e32 v48, s28, v199
	v_add_u32_e32 v82, v48, v207
	ds_read_b128 v[78:81], v82
	ds_read_b128 v[96:99], v82 offset:4096
	s_waitcnt lgkmcnt(12)
	v_mfma_f32_32x32x16_f16 v[16:31], v[136:139], v[168:171], v[16:31]
	v_exp_f32_e32 v58, v58
	v_exp_f32_e32 v59, v59
	v_exp_f32_e32 v60, v60
	v_exp_f32_e32 v61, v61
	v_add_u32_e32 v82, v48, v206
	ds_read_b128 v[172:175], v82
	ds_read_b128 v[168:171], v82 offset:4096
	s_waitcnt lgkmcnt(12)
	v_mfma_f32_32x32x16_f16 v[0:15], v[136:139], v[164:167], v[0:15]
	v_exp_f32_e32 v62, v62
	v_exp_f32_e32 v63, v63
	v_exp_f32_e32 v64, v64
	v_exp_f32_e32 v65, v65
	v_add_u32_e32 v82, v48, v205
	ds_read_b128 v[164:167], v82
	ds_read_b128 v[156:159], v82 offset:4096
	s_waitcnt lgkmcnt(12)
	v_mfma_f32_32x32x16_f16 v[16:31], v[132:135], v[70:73], v[16:31]
	v_exp_f32_e32 v32, v32
	v_exp_f32_e32 v33, v33
	v_exp_f32_e32 v34, v34
	v_exp_f32_e32 v35, v35
	v_add_u32_e32 v48, v48, v204
	ds_read_b128 v[160:163], v48
	ds_read_b128 v[70:73], v48 offset:4096
	s_waitcnt lgkmcnt(12)
	v_mfma_f32_32x32x16_f16 v[0:15], v[132:135], v[66:69], v[0:15]
	v_exp_f32_e32 v36, v36
	v_exp_f32_e32 v37, v37
	v_exp_f32_e32 v38, v38
	v_exp_f32_e32 v39, v39
	s_waitcnt lgkmcnt(10)
	v_mfma_f32_32x32x16_f16 v[16:31], v[128:131], v[74:77], v[16:31]
	v_exp_f32_e32 v40, v40
	v_exp_f32_e32 v41, v41
	v_exp_f32_e32 v42, v42
	v_exp_f32_e32 v43, v43
	s_waitcnt lgkmcnt(8)
	v_mfma_f32_32x32x16_f16 v[0:15], v[128:131], v[148:151], v[0:15]
	v_exp_f32_e32 v44, v44
	v_exp_f32_e32 v45, v45
	v_exp_f32_e32 v46, v46
	v_exp_f32_e32 v47, v47
	s_waitcnt vmcnt(8) lgkmcnt(0)
	s_barrier
	s_andn2_b64 vcc, exec, s[20:21]
	s_cbranch_vccnz .LBB1_67
	ds_read_b128 v[66:69], v183 offset:96
	ds_read_b128 v[74:77], v183 offset:64
	ds_read_b128 v[82:85], v183 offset:32
	ds_read_b128 v[86:89], v183
	s_waitcnt lgkmcnt(3)
	v_pk_mul_f32 v[30:31], v[30:31], v[68:69]
	s_waitcnt lgkmcnt(2)
	v_pk_mul_f32 v[26:27], v[26:27], v[76:77]
	s_waitcnt lgkmcnt(1)
	v_pk_mul_f32 v[22:23], v[22:23], v[84:85]
	s_waitcnt lgkmcnt(0)
	v_pk_mul_f32 v[18:19], v[18:19], v[88:89]
	v_pk_mul_f32 v[28:29], v[28:29], v[66:67]
	v_pk_mul_f32 v[24:25], v[24:25], v[74:75]
	v_pk_mul_f32 v[20:21], v[20:21], v[82:83]
	v_pk_mul_f32 v[16:17], v[16:17], v[86:87]
	v_pk_mul_f32 v[14:15], v[14:15], v[68:69]
	v_pk_mul_f32 v[10:11], v[10:11], v[76:77]
	v_pk_mul_f32 v[6:7], v[6:7], v[84:85]
	v_pk_mul_f32 v[2:3], v[2:3], v[88:89]
	v_pk_mul_f32 v[12:13], v[12:13], v[66:67]
	v_pk_mul_f32 v[8:9], v[8:9], v[74:75]
	v_pk_mul_f32 v[4:5], v[4:5], v[82:83]
	v_pk_mul_f32 v[0:1], v[0:1], v[86:87]
.LBB1_67:
	s_add_i32 s4, s28, 0x4000
	s_cmpk_lg_u32 s28, 0x8000
	s_cselect_b32 s20, s4, 0
	v_add_u32_e32 v48, s35, v197
	ds_read_b64_tr_b16 v[144:145], v48 offset:49152
	ds_read_b64_tr_b16 v[146:147], v48 offset:49664
	s_waitcnt lgkmcnt(9)
	v_mfma_f32_32x32x16_f16 v[80:95], v[78:81], v[124:127], 0
	v_add_f32_e32 v66, v50, v51
	v_add_f32_e32 v66, v52, v66
	v_add_f32_e32 v66, v53, v66
	v_add_f32_e32 v66, v54, v66
	v_add_f32_e32 v66, v55, v66
	v_cvt_pk_f16_f32 v140, v50, v51
	v_cvt_pk_f16_f32 v141, v52, v53
	s_nop 0
	ds_read_b64_tr_b16 v[152:153], v48 offset:53248
	ds_read_b64_tr_b16 v[154:155], v48 offset:53760
	s_waitcnt lgkmcnt(10)
	v_mfma_f32_32x32x16_f16 v[96:111], v[96:99], v[124:127], 0
	v_add_f32_e32 v50, v56, v66
	v_add_f32_e32 v50, v57, v50
	v_add_f32_e32 v50, v58, v50
	v_add_f32_e32 v50, v59, v50
	v_cvt_pk_f16_f32 v142, v54, v55
	v_cvt_pk_f16_f32 v143, v56, v57
	s_nop 0
	ds_read_b64_tr_b16 v[148:149], v48 offset:50176
	ds_read_b64_tr_b16 v[150:151], v48 offset:50688
	s_waitcnt lgkmcnt(11)
	v_mfma_f32_32x32x16_f16 v[80:95], v[172:175], v[120:123], v[80:95]
	v_add_f32_e32 v50, v60, v50
	v_add_f32_e32 v50, v61, v50
	v_add_f32_e32 v50, v62, v50
	v_add_f32_e32 v50, v63, v50
	v_cvt_pk_f16_f32 v136, v58, v59
	v_cvt_pk_f16_f32 v137, v60, v61
	s_nop 0
	ds_read_b64_tr_b16 v[58:59], v48 offset:54272
	ds_read_b64_tr_b16 v[60:61], v48 offset:54784
	s_waitcnt lgkmcnt(12)
	v_mfma_f32_32x32x16_f16 v[96:111], v[168:171], v[120:123], v[96:111]
	v_add_f32_e32 v50, v64, v50
	v_add_f32_e32 v50, v65, v50
	v_add_f32_e32 v50, v32, v50
	v_add_f32_e32 v50, v33, v50
	v_cvt_pk_f16_f32 v138, v62, v63
	v_cvt_pk_f16_f32 v139, v64, v65
	s_nop 0
	ds_read_b64_tr_b16 v[54:55], v48 offset:51200
	ds_read_b64_tr_b16 v[56:57], v48 offset:51712
	s_waitcnt lgkmcnt(13)
	v_mfma_f32_32x32x16_f16 v[80:95], v[164:167], v[116:119], v[80:95]
	v_add_f32_e32 v50, v34, v50
	v_add_f32_e32 v50, v35, v50
	v_add_f32_e32 v50, v36, v50
	v_add_f32_e32 v62, v37, v50
	v_cvt_pk_f16_f32 v132, v32, v33
	v_cvt_pk_f16_f32 v133, v34, v35
	s_nop 0
	ds_read_b64_tr_b16 v[50:51], v48 offset:55296
	ds_read_b64_tr_b16 v[52:53], v48 offset:55808
	s_waitcnt lgkmcnt(14)
	v_mfma_f32_32x32x16_f16 v[96:111], v[156:159], v[116:119], v[96:111]
	v_add_f32_e32 v32, v38, v62
	v_add_f32_e32 v32, v39, v32
	v_add_f32_e32 v32, v40, v32
	v_add_f32_e32 v32, v41, v32
	v_cvt_pk_f16_f32 v134, v36, v37
	v_cvt_pk_f16_f32 v135, v38, v39
	s_nop 0
	ds_read_b64_tr_b16 v[168:169], v48 offset:52224
	ds_read_b64_tr_b16 v[170:171], v48 offset:52736
	s_waitcnt lgkmcnt(14)
	v_mfma_f32_32x32x16_f16 v[80:95], v[160:163], v[112:115], v[80:95]
	v_add_f32_e32 v32, v42, v32
	v_add_f32_e32 v32, v43, v32
	v_add_f32_e32 v32, v44, v32
	v_add_f32_e32 v32, v45, v32
	v_cvt_pk_f16_f32 v128, v40, v41
	v_cvt_pk_f16_f32 v129, v42, v43
	s_nop 0
	ds_read_b64_tr_b16 v[172:173], v48 offset:56320
	ds_read_b64_tr_b16 v[174:175], v48 offset:56832
	v_mfma_f32_32x32x16_f16 v[96:111], v[70:73], v[112:115], v[96:111]
	v_add_f32_e32 v32, v46, v32
	v_add_f32_e32 v32, v47, v32
	v_add_f32_e32 v48, 0, v32
	v_cvt_pk_f16_f32 v130, v44, v45
	v_cvt_pk_f16_f32 v131, v46, v47
	s_nop 0
	s_min_u32 s4, s36, s33
	s_lshl_b32 s4, s4, 18
	v_lshl_add_u64 v[32:33], v[194:195], 0, s[4:5]
	s_add_i32 s4, s28, s29
	s_bitcmp1_b32 s54, 8
	s_cbranch_scc1 .Ldmaskip_37
	s_mov_b32 s21, m0
	s_mov_b32 m0, s4
	s_nop 0
	global_load_lds_dwordx4 v[32:33], off
	s_mov_b32 m0, s21
	s_cmp_ge_u32 s4, 0xc000
	s_cselect_b32 s56, 64, 0x10000
	v_lshl_add_u64 v[220:221], v[32:33], 0, s[56:57]
	s_add_i32 s55, s4, 0x1000
	s_mov_b32 m0, s55
	s_nop 0
	global_load_lds_dwordx4 v[220:221], off
.Ldmaskip_37:
	v_lshl_add_u64 v[32:33], v[32:33], 0, s[6:7]
	s_addk_i32 s4, 0x2000
	s_bitcmp1_b32 s54, 8
	s_cbranch_scc1 .Ldmaskip_38
	s_mov_b32 s21, m0
	s_mov_b32 m0, s4
	s_nop 0
	global_load_lds_dwordx4 v[32:33], off
	s_mov_b32 m0, s21
	s_cmp_ge_u32 s4, 0xc000
	s_cselect_b32 s56, 64, 0x10000
	v_lshl_add_u64 v[220:221], v[32:33], 0, s[56:57]
	s_add_i32 s55, s4, 0x1000
	s_mov_b32 m0, s55
	s_nop 0
	global_load_lds_dwordx4 v[220:221], off
.Ldmaskip_38:
	v_lshl_add_u64 v[32:33], v[180:181], 0, s[14:15]
	s_add_i32 s4, s20, s31
	s_bitcmp1_b32 s54, 8
	s_cbranch_scc1 .Ldmaskip_39
	s_mov_b32 s21, m0
	s_mov_b32 m0, s4
	s_nop 0
	global_load_lds_dwordx4 v[32:33], off
	s_mov_b32 m0, s21
	s_cmp_ge_u32 s4, 0xc000
	s_cselect_b32 s56, 64, 0x10000
	v_lshl_add_u64 v[220:221], v[32:33], 0, s[56:57]
	s_add_i32 s55, s4, 0x1000
	s_mov_b32 m0, s55
	s_nop 0
	global_load_lds_dwordx4 v[220:221], off
.Ldmaskip_39:
	v_lshl_add_u64 v[32:33], v[180:181], 0, s[16:17]
	s_addk_i32 s4, 0x2000
	s_bitcmp1_b32 s54, 8
	s_cbranch_scc1 .Ldmaskip_40
	s_mov_b32 s21, m0
	s_mov_b32 m0, s4
	s_nop 0
	global_load_lds_dwordx4 v[32:33], off
	s_mov_b32 m0, s21
	s_cmp_ge_u32 s4, 0xc000
	s_cselect_b32 s56, 64, 0x10000
	v_lshl_add_u64 v[220:221], v[32:33], 0, s[56:57]
	s_add_i32 s55, s4, 0x1000
	s_mov_b32 m0, s55
	s_nop 0
	global_load_lds_dwordx4 v[220:221], off
.Ldmaskip_40:
	s_andn2_b64 vcc, exec, s[18:19]
	s_mov_b64 s[18:19], -1
	s_cbranch_vccz .LBB1_80
	s_andn2_b64 vcc, exec, s[18:19]
	s_cbranch_vccnz .LBB1_71

.LBB1_72:
	s_waitcnt lgkmcnt(14)
	v_mfma_f32_32x32x16_f16 v[16:31], v[140:143], v[144:147], v[16:31]
	v_exp_f32_e32 v64, v64
	v_exp_f32_e32 v65, v65
	v_exp_f32_e32 v66, v62
	v_exp_f32_e32 v67, v63
	s_waitcnt lgkmcnt(12)
	v_mfma_f32_32x32x16_f16 v[0:15], v[140:143], v[152:155], v[0:15]
	v_exp_f32_e32 v68, v68
	v_exp_f32_e32 v69, v69
	v_exp_f32_e32 v70, v70
	v_exp_f32_e32 v71, v71
	v_add_u32_e32 v48, s20, v199
	v_add_u32_e32 v62, v48, v207
	ds_read_b128 v[80:83], v62
	ds_read_b128 v[96:99], v62 offset:4096
	s_waitcnt lgkmcnt(12)
	v_mfma_f32_32x32x16_f16 v[16:31], v[136:139], v[148:151], v[16:31]
	v_exp_f32_e32 v72, v72
	v_exp_f32_e32 v73, v73
	v_exp_f32_e32 v74, v74
	v_exp_f32_e32 v75, v75
	v_add_u32_e32 v62, v48, v206
	ds_read_b128 v[164:167], v62
	ds_read_b128 v[160:163], v62 offset:4096
	s_waitcnt lgkmcnt(12)
	v_mfma_f32_32x32x16_f16 v[0:15], v[136:139], v[58:61], v[0:15]
	v_exp_f32_e32 v76, v76
	v_exp_f32_e32 v77, v77
	v_exp_f32_e32 v78, v78
	v_exp_f32_e32 v79, v79
	v_add_u32_e32 v58, v48, v205
	ds_read_b128 v[156:159], v58
	ds_read_b128 v[152:155], v58 offset:4096
	s_waitcnt lgkmcnt(12)
	v_mfma_f32_32x32x16_f16 v[16:31], v[132:135], v[54:57], v[16:31]
	v_exp_f32_e32 v32, v32
	v_exp_f32_e32 v33, v33
	v_exp_f32_e32 v34, v34
	v_exp_f32_e32 v35, v35
	v_add_u32_e32 v48, v48, v204
	ds_read_b128 v[148:151], v48
	ds_read_b128 v[144:147], v48 offset:4096
	s_waitcnt lgkmcnt(12)
	v_mfma_f32_32x32x16_f16 v[0:15], v[132:135], v[50:53], v[0:15]
	v_exp_f32_e32 v36, v36
	v_exp_f32_e32 v37, v37
	v_exp_f32_e32 v38, v38
	v_exp_f32_e32 v39, v39
	s_waitcnt lgkmcnt(10)
	v_mfma_f32_32x32x16_f16 v[16:31], v[128:131], v[168:171], v[16:31]
	v_exp_f32_e32 v40, v40
	v_exp_f32_e32 v41, v41
	v_exp_f32_e32 v42, v42
	v_exp_f32_e32 v43, v43
	s_waitcnt lgkmcnt(8)
	v_mfma_f32_32x32x16_f16 v[0:15], v[128:131], v[172:175], v[0:15]
	v_exp_f32_e32 v44, v44
	v_exp_f32_e32 v45, v45
	v_exp_f32_e32 v46, v46
	v_exp_f32_e32 v47, v47
	s_waitcnt vmcnt(8) lgkmcnt(0)
	s_barrier
	s_andn2_b64 vcc, exec, s[18:19]
	s_cbranch_vccnz .LBB1_74
	ds_read_b128 v[50:53], v183 offset:96
	ds_read_b128 v[54:57], v183 offset:64
	ds_read_b128 v[58:61], v183 offset:32
	ds_read_b128 v[84:87], v183
	s_waitcnt lgkmcnt(3)
	v_pk_mul_f32 v[30:31], v[30:31], v[52:53]
	s_waitcnt lgkmcnt(2)
	v_pk_mul_f32 v[26:27], v[26:27], v[56:57]
	s_waitcnt lgkmcnt(1)
	v_pk_mul_f32 v[22:23], v[22:23], v[60:61]
	s_waitcnt lgkmcnt(0)
	v_pk_mul_f32 v[18:19], v[18:19], v[86:87]
	v_pk_mul_f32 v[28:29], v[28:29], v[50:51]
	v_pk_mul_f32 v[24:25], v[24:25], v[54:55]
	v_pk_mul_f32 v[20:21], v[20:21], v[58:59]
	v_pk_mul_f32 v[16:17], v[16:17], v[84:85]
	v_pk_mul_f32 v[14:15], v[14:15], v[52:53]
	v_pk_mul_f32 v[10:11], v[10:11], v[56:57]
	v_pk_mul_f32 v[6:7], v[6:7], v[60:61]
	v_pk_mul_f32 v[2:3], v[2:3], v[86:87]
	v_pk_mul_f32 v[12:13], v[12:13], v[50:51]
	v_pk_mul_f32 v[8:9], v[8:9], v[54:55]
	v_pk_mul_f32 v[4:5], v[4:5], v[58:59]
	v_pk_mul_f32 v[0:1], v[0:1], v[84:85]

.LBB1_90:
	s_mov_b64 s[4:5], -1
	s_xor_b64 s[6:7], s[2:3], -1
	v_add_u32_e32 v48, s30, v197
	ds_read_b64_tr_b16 v[54:55], v48 offset:49152
	ds_read_b64_tr_b16 v[56:57], v48 offset:49664
	s_waitcnt lgkmcnt(9)
	v_mfma_f32_32x32x16_f16 v[80:95], v[80:83], v[124:127], 0
	v_add_f32_e32 v50, v64, v65
	v_add_f32_e32 v50, v66, v50
	v_add_f32_e32 v50, v67, v50
	v_add_f32_e32 v50, v68, v50
	v_add_f32_e32 v50, v69, v50
	v_cvt_pk_f16_f32 v140, v64, v65
	v_cvt_pk_f16_f32 v141, v66, v67
	s_mov_b32 s9, 0
	ds_read_b64_tr_b16 v[184:185], v48 offset:53248
	ds_read_b64_tr_b16 v[186:187], v48 offset:53760
	s_waitcnt lgkmcnt(10)
	v_mfma_f32_32x32x16_f16 v[96:111], v[96:99], v[124:127], 0
	v_add_f32_e32 v50, v70, v50
	v_add_f32_e32 v50, v71, v50
	v_add_f32_e32 v50, v72, v50
	v_add_f32_e32 v50, v73, v50
	v_cvt_pk_f16_f32 v142, v68, v69
	v_cvt_pk_f16_f32 v143, v70, v71
	s_nop 0
	ds_read_b64_tr_b16 v[176:177], v48 offset:50176
	ds_read_b64_tr_b16 v[178:179], v48 offset:50688
	s_waitcnt lgkmcnt(11)
	v_mfma_f32_32x32x16_f16 v[80:95], v[164:167], v[120:123], v[80:95]
	v_add_f32_e32 v50, v74, v50
	v_add_f32_e32 v50, v75, v50
	v_add_f32_e32 v50, v76, v50
	v_add_f32_e32 v50, v77, v50
	v_cvt_pk_f16_f32 v136, v72, v73
	v_cvt_pk_f16_f32 v137, v74, v75
	s_nop 0
	ds_read_b64_tr_b16 v[168:169], v48 offset:54272
	ds_read_b64_tr_b16 v[170:171], v48 offset:54784
	s_waitcnt lgkmcnt(12)
	v_mfma_f32_32x32x16_f16 v[96:111], v[160:163], v[120:123], v[96:111]
	v_add_f32_e32 v50, v78, v50
	v_add_f32_e32 v50, v79, v50
	v_add_f32_e32 v50, v32, v50
	v_add_f32_e32 v50, v33, v50
	v_cvt_pk_f16_f32 v138, v76, v77
	v_cvt_pk_f16_f32 v139, v78, v79
	s_nop 0
	ds_read_b64_tr_b16 v[58:59], v48 offset:51200
	ds_read_b64_tr_b16 v[60:61], v48 offset:51712
	s_waitcnt lgkmcnt(13)
	v_mfma_f32_32x32x16_f16 v[80:95], v[156:159], v[116:119], v[80:95]
	v_add_f32_e32 v50, v34, v50
	v_add_f32_e32 v50, v35, v50
	v_add_f32_e32 v50, v36, v50
	v_add_f32_e32 v62, v37, v50
	v_cvt_pk_f16_f32 v132, v32, v33
	v_cvt_pk_f16_f32 v133, v34, v35
	s_nop 0
	ds_read_b64_tr_b16 v[50:51], v48 offset:55296
	ds_read_b64_tr_b16 v[52:53], v48 offset:55808
	s_waitcnt lgkmcnt(14)
	v_mfma_f32_32x32x16_f16 v[96:111], v[152:155], v[116:119], v[96:111]
	v_add_f32_e32 v32, v38, v62
	v_add_f32_e32 v32, v39, v32
	v_add_f32_e32 v32, v40, v32
	v_add_f32_e32 v32, v41, v32
	v_cvt_pk_f16_f32 v134, v36, v37
	v_cvt_pk_f16_f32 v135, v38, v39
	s_nop 0
	ds_read_b64_tr_b16 v[172:173], v48 offset:52224
	ds_read_b64_tr_b16 v[174:175], v48 offset:52736
	s_waitcnt lgkmcnt(14)
	v_mfma_f32_32x32x16_f16 v[80:95], v[148:151], v[112:115], v[80:95]
	v_add_f32_e32 v32, v42, v32
	v_add_f32_e32 v32, v43, v32
	v_add_f32_e32 v32, v44, v32
	v_add_f32_e32 v32, v45, v32
	v_cvt_pk_f16_f32 v128, v40, v41
	v_cvt_pk_f16_f32 v129, v42, v43
	s_nop 0
	ds_read_b64_tr_b16 v[180:181], v48 offset:56320
	ds_read_b64_tr_b16 v[182:183], v48 offset:56832
	v_mfma_f32_32x32x16_f16 v[96:111], v[144:147], v[112:115], v[96:111]
	v_add_f32_e32 v32, v46, v32
	v_add_f32_e32 v32, v47, v32
	v_add_f32_e32 v48, 0, v32
	v_cvt_pk_f16_f32 v130, v44, v45
	v_cvt_pk_f16_f32 v131, v46, v47
	s_nop 0
	s_lshl_b32 s8, s33, 18
	v_lshl_add_u64 v[32:33], v[194:195], 0, s[8:9]
	s_add_i32 s8, s35, s29
	s_bitcmp1_b32 s54, 8
	s_cbranch_scc1 .Ldmaskip_41
	s_mov_b32 s14, m0
	s_mov_b32 m0, s8
	s_nop 0
	global_load_lds_dwordx4 v[32:33], off
	s_mov_b32 m0, s14
	s_cmp_ge_u32 s8, 0xc000
	s_cselect_b32 s56, 64, 0x10000
	v_lshl_add_u64 v[220:221], v[32:33], 0, s[56:57]
	s_add_i32 s55, s8, 0x1000
	s_mov_b32 m0, s55
	s_nop 0
	global_load_lds_dwordx4 v[220:221], off
.Ldmaskip_41:
	s_mov_b64 s[14:15], 0x20000
	s_addk_i32 s8, 0x2000
	v_lshl_add_u64 v[32:33], v[32:33], 0, s[14:15]
	s_bitcmp1_b32 s54, 8
	s_cbranch_scc1 .Ldmaskip_42
	s_mov_b32 s14, m0
	s_mov_b32 m0, s8
	s_nop 0
	global_load_lds_dwordx4 v[32:33], off
	s_mov_b32 m0, s14
	s_cmp_ge_u32 s8, 0xc000
	s_cselect_b32 s56, 64, 0x10000
	v_lshl_add_u64 v[220:221], v[32:33], 0, s[56:57]
	s_add_i32 s55, s8, 0x1000
	s_mov_b32 m0, s55
	s_nop 0
	global_load_lds_dwordx4 v[220:221], off
.Ldmaskip_42:
	s_lshl_b32 s8, s18, 18
	v_lshl_add_u64 v[32:33], v[190:191], 0, s[8:9]
	s_mov_b64 s[8:9], 0x40000
	v_lshl_add_u64 v[34:35], v[32:33], 0, s[8:9]
	s_add_i32 s14, s28, s31
	s_bitcmp1_b32 s54, 8
	s_cbranch_scc1 .Ldmaskip_43
	s_mov_b32 s8, m0
	s_mov_b32 m0, s14
	s_nop 0
	global_load_lds_dwordx4 v[34:35], off
	s_mov_b32 m0, s8
	s_cmp_ge_u32 s14, 0xc000
	s_cselect_b32 s56, 64, 0x10000
	v_lshl_add_u64 v[220:221], v[34:35], 0, s[56:57]
	s_add_i32 s55, s14, 0x1000
	s_mov_b32 m0, s55
	s_nop 0
	global_load_lds_dwordx4 v[220:221], off
.Ldmaskip_43:
	s_mov_b64 s[8:9], 0x60000
	v_lshl_add_u64 v[32:33], v[32:33], 0, s[8:9]
	s_add_i32 s8, s14, 0x2000
	s_andn2_b64 vcc, exec, s[6:7]
	s_bitcmp1_b32 s54, 8
	s_cbranch_scc1 .Ldmaskip_44
	s_mov_b32 s6, m0
	s_mov_b32 m0, s8
	s_nop 0
	global_load_lds_dwordx4 v[32:33], off
	s_mov_b32 m0, s6
	s_cmp_ge_u32 s8, 0xc000
	s_cselect_b32 s56, 64, 0x10000
	v_lshl_add_u64 v[220:221], v[32:33], 0, s[56:57]
	s_add_i32 s55, s8, 0x1000
	s_mov_b32 m0, s55
	s_nop 0
	global_load_lds_dwordx4 v[220:221], off
.Ldmaskip_44:
	s_cbranch_vccz .LBB1_130
	s_andn2_b64 vcc, exec, s[4:5]
	s_cbranch_vccnz .LBB1_94

.LBB1_95:
	s_waitcnt lgkmcnt(14)
	v_mfma_f32_32x32x16_f16 v[16:31], v[140:143], v[54:57], v[16:31]
	v_exp_f32_e32 v64, v64
	v_exp_f32_e32 v65, v65
	v_exp_f32_e32 v66, v62
	v_exp_f32_e32 v67, v63
	s_waitcnt lgkmcnt(12)
	v_mfma_f32_32x32x16_f16 v[0:15], v[140:143], v[184:187], v[0:15]
	v_exp_f32_e32 v68, v68
	v_exp_f32_e32 v69, v69
	v_exp_f32_e32 v70, v70
	v_exp_f32_e32 v71, v71
	v_add_u32_e32 v48, s28, v199
	v_add_u32_e32 v54, v48, v207
	ds_read_b128 v[80:83], v54
	ds_read_b128 v[96:99], v54 offset:4096
	s_waitcnt lgkmcnt(12)
	v_mfma_f32_32x32x16_f16 v[16:31], v[136:139], v[176:179], v[16:31]
	v_exp_f32_e32 v72, v72
	v_exp_f32_e32 v73, v73
	v_exp_f32_e32 v74, v74
	v_exp_f32_e32 v75, v75
	v_add_u32_e32 v54, v48, v206
	ds_read_b128 v[164:167], v54
	ds_read_b128 v[160:163], v54 offset:4096
	s_waitcnt lgkmcnt(12)
	v_mfma_f32_32x32x16_f16 v[0:15], v[136:139], v[168:171], v[0:15]
	v_exp_f32_e32 v76, v76
	v_exp_f32_e32 v77, v77
	v_exp_f32_e32 v78, v78
	v_exp_f32_e32 v79, v79
	v_add_u32_e32 v54, v48, v205
	ds_read_b128 v[156:159], v54
	ds_read_b128 v[152:155], v54 offset:4096
	s_waitcnt lgkmcnt(12)
	v_mfma_f32_32x32x16_f16 v[16:31], v[132:135], v[58:61], v[16:31]
	v_exp_f32_e32 v32, v32
	v_exp_f32_e32 v33, v33
	v_exp_f32_e32 v34, v34
	v_exp_f32_e32 v35, v35
	v_add_u32_e32 v48, v48, v204
	ds_read_b128 v[148:151], v48
	ds_read_b128 v[144:147], v48 offset:4096
	s_waitcnt lgkmcnt(12)
	v_mfma_f32_32x32x16_f16 v[0:15], v[132:135], v[50:53], v[0:15]
	v_exp_f32_e32 v36, v36
	v_exp_f32_e32 v37, v37
	v_exp_f32_e32 v38, v38
	v_exp_f32_e32 v39, v39
	s_waitcnt lgkmcnt(10)
	v_mfma_f32_32x32x16_f16 v[16:31], v[128:131], v[172:175], v[16:31]
	v_exp_f32_e32 v40, v40
	v_exp_f32_e32 v41, v41
	v_exp_f32_e32 v42, v42
	v_exp_f32_e32 v43, v43
	s_waitcnt lgkmcnt(8)
	v_mfma_f32_32x32x16_f16 v[0:15], v[128:131], v[180:183], v[0:15]
	v_exp_f32_e32 v44, v44
	v_exp_f32_e32 v45, v45
	v_exp_f32_e32 v46, v46
	v_exp_f32_e32 v47, v47
	s_waitcnt vmcnt(8) lgkmcnt(0)
	s_barrier
	s_andn2_b64 vcc, exec, s[4:5]
	s_cbranch_vccnz .LBB1_97
	v_lshl_add_u32 v48, v203, 2, s27
	ds_read_b128 v[50:53], v48 offset:96
	ds_read_b128 v[54:57], v48 offset:64
	ds_read_b128 v[58:61], v48 offset:32
	ds_read_b128 v[84:87], v48
	s_waitcnt lgkmcnt(3)
	v_pk_mul_f32 v[30:31], v[30:31], v[52:53]
	s_waitcnt lgkmcnt(2)
	v_pk_mul_f32 v[26:27], v[26:27], v[56:57]
	s_waitcnt lgkmcnt(1)
	v_pk_mul_f32 v[22:23], v[22:23], v[60:61]
	s_waitcnt lgkmcnt(0)
	v_pk_mul_f32 v[18:19], v[18:19], v[86:87]
	v_pk_mul_f32 v[28:29], v[28:29], v[50:51]
	v_pk_mul_f32 v[24:25], v[24:25], v[54:55]
	v_pk_mul_f32 v[20:21], v[20:21], v[58:59]
	v_pk_mul_f32 v[16:17], v[16:17], v[84:85]
	v_pk_mul_f32 v[14:15], v[14:15], v[52:53]
	v_pk_mul_f32 v[10:11], v[10:11], v[56:57]
	v_pk_mul_f32 v[6:7], v[6:7], v[60:61]
	v_pk_mul_f32 v[2:3], v[2:3], v[86:87]
	v_pk_mul_f32 v[12:13], v[12:13], v[50:51]
	v_pk_mul_f32 v[8:9], v[8:9], v[54:55]
	v_pk_mul_f32 v[4:5], v[4:5], v[58:59]
	v_pk_mul_f32 v[0:1], v[0:1], v[84:85]

	.amdhsa_kernel _Z10attn64_fwdPKDF16_S0_S0_PDF16_
		.amdhsa_group_segment_fixed_size 0
		.amdhsa_private_segment_fixed_size 0
		.amdhsa_kernarg_size 32
		.amdhsa_user_sgpr_count 2
		.amdhsa_user_sgpr_dispatch_ptr 0
		.amdhsa_user_sgpr_queue_ptr 0
		.amdhsa_user_sgpr_kernarg_segment_ptr 1
		.amdhsa_user_sgpr_dispatch_id 0
		.amdhsa_user_sgpr_kernarg_preload_length 0
		.amdhsa_user_sgpr_kernarg_preload_offset 0
		.amdhsa_user_sgpr_private_segment_size 0
		.amdhsa_uses_dynamic_stack 0
		.amdhsa_enable_private_segment 0
		.amdhsa_system_sgpr_workgroup_id_x 1
		.amdhsa_system_sgpr_workgroup_id_y 0
		.amdhsa_system_sgpr_workgroup_id_z 0
		.amdhsa_system_sgpr_workgroup_info 0
		.amdhsa_system_vgpr_workitem_id 0
		.amdhsa_next_free_vgpr 222
		.amdhsa_next_free_sgpr 58
		.amdhsa_accum_offset 224
		.amdhsa_reserve_vcc 1
		.amdhsa_float_round_mode_32 0
		.amdhsa_float_round_mode_16_64 0
		.amdhsa_float_denorm_mode_32 3
		.amdhsa_float_denorm_mode_16_64 3
		.amdhsa_dx10_clamp 1
		.amdhsa_ieee_mode 1
		.amdhsa_fp16_overflow 0
		.amdhsa_tg_split 0
		.amdhsa_exception_fp_ieee_invalid_op 0
		.amdhsa_exception_fp_denorm_src 0
		.amdhsa_exception_fp_ieee_div_zero 0
		.amdhsa_exception_fp_ieee_overflow 0
		.amdhsa_exception_fp_ieee_underflow 0
		.amdhsa_exception_fp_ieee_inexact 0
		.amdhsa_exception_int_div_zero 0
	.end_amdhsa_kernel

amdhsa.kernels:
  - .agpr_count:     0
    .args:
      - .address_space:  global
        .offset:         0
        .size:           8
        .value_kind:     global_buffer
      - .address_space:  global
        .offset:         8
        .size:           8
        .value_kind:     global_buffer
      - .address_space:  global
        .offset:         16
        .size:           8
        .value_kind:     global_buffer
      - .address_space:  global
        .offset:         24
        .size:           8
        .value_kind:     global_buffer
      - .address_space:  global
        .offset:         32
        .size:           8
        .value_kind:     global_buffer
      - .address_space:  global
        .offset:         40
        .size:           8
        .value_kind:     global_buffer
      - .address_space:  global
        .offset:         48
        .size:           8
        .value_kind:     global_buffer
      - .address_space:  global
        .offset:         56
        .size:           8
        .value_kind:     global_buffer
    .group_segment_fixed_size: 0
    .kernarg_segment_align: 8
    .kernarg_segment_size: 64
    .language:       OpenCL C
    .language_version:
      - 2
      - 0
    .max_flat_workgroup_size: 256
    .name:           _Z10cvt_kernelPKfS0_S0_S0_S0_PDF16_S1_S1_
    .private_segment_fixed_size: 0
    .sgpr_count:     20
    .sgpr_spill_count: 0
    .symbol:         _Z10cvt_kernelPKfS0_S0_S0_S0_PDF16_S1_S1_.kd
    .uniform_work_group_size: 1
    .uses_dynamic_stack: false
    .vgpr_count:     70
    .vgpr_spill_count: 0
    .wavefront_size: 64
  - .agpr_count:     0
    .args:
      - .address_space:  global
        .offset:         0
        .size:           8
        .value_kind:     global_buffer
      - .address_space:  global
        .offset:         8
        .size:           8
        .value_kind:     global_buffer
      - .address_space:  global
        .offset:         16
        .size:           8
        .value_kind:     global_buffer
      - .address_space:  global
        .offset:         24
        .size:           8
        .value_kind:     global_buffer
    .group_segment_fixed_size: 0
    .kernarg_segment_align: 8
    .kernarg_segment_size: 32
    .language:       OpenCL C
    .language_version:
      - 2
      - 0
    .max_flat_workgroup_size: 512
    .name:           _Z10attn64_fwdPKDF16_S0_S0_PDF16_
    .private_segment_fixed_size: 0
    .sgpr_count:     64
    .sgpr_spill_count: 0
    .symbol:         _Z10attn64_fwdPKDF16_S0_S0_PDF16_.kd
    .uniform_work_group_size: 1
    .uses_dynamic_stack: false
    .vgpr_count:     222
    .vgpr_spill_count: 0
    .wavefront_size: 64
  - .agpr_count:     0
    .args:
      - .address_space:  global
        .offset:         0
        .size:           8
        .value_kind:     global_buffer
      - .address_space:  global
        .offset:         8
        .size:           8
        .value_kind:     global_buffer
      - .address_space:  global
        .offset:         16
        .size:           8
        .value_kind:     global_buffer
      - .actual_access:  read_only
        .address_space:  global
        .offset:         24
        .size:           8
        .value_kind:     global_buffer
      - .offset:         32
        .size:           4
        .value_kind:     by_value
    .group_segment_fixed_size: 0
    .kernarg_segment_align: 8
    .kernarg_segment_size: 36
    .language:       OpenCL C
    .language_version:
      - 2
      - 0
    .max_flat_workgroup_size: 512
    .name:           _Z8gemm16_kILi256ELi192ELi0ELi2EEvPKDF16_S1_PvPKfi
    .private_segment_fixed_size: 0
    .sgpr_count:     30
    .sgpr_spill_count: 0
    .symbol:         _Z8gemm16_kILi256ELi192ELi0ELi2EEvPKDF16_S1_PvPKfi.kd
    .uniform_work_group_size: 1
    .uses_dynamic_stack: false
    .vgpr_count:     208
    .vgpr_spill_count: 0
    .wavefront_size: 64
  - .agpr_count:     0
    .args:
      - .address_space:  global
        .offset:         0
        .size:           8
        .value_kind:     global_buffer
      - .address_space:  global
        .offset:         8
        .size:           8
        .value_kind:     global_buffer
      - .address_space:  global
        .offset:         16
        .size:           8
        .value_kind:     global_buffer
      - .actual_access:  read_only
        .address_space:  global
        .offset:         24
        .size:           8
        .value_kind:     global_buffer
      - .offset:         32
        .size:           4
        .value_kind:     by_value
    .group_segment_fixed_size: 0
    .kernarg_segment_align: 8
    .kernarg_segment_size: 36
    .language:       OpenCL C
    .language_version:
      - 2
      - 0
    .max_flat_workgroup_size: 512
    .name:           _Z8gemm16_kILi128ELi128ELi1ELi3EEvPKDF16_S1_PvPKfi
    .private_segment_fixed_size: 0
    .sgpr_count:     28
    .sgpr_spill_count: 0
    .symbol:         _Z8gemm16_kILi128ELi128ELi1ELi3EEvPKDF16_S1_PvPKfi.kd
    .uniform_work_group_size: 1
    .uses_dynamic_stack: false
    .vgpr_count:     104
    .vgpr_spill_count: 0
    .wavefront_size: 64
